# all w_down conversion moved out of the scan phase into the gate/up phase (XP5 0)
# baseline (speedup 1.0000x reference)
; #define LAS __attribute__((address_space(3)))
; __device__ __forceinline__ void cvt_item_lds(const float* src, int ld_src, fp8_t* dst, int ld_dst, LAS unsigned char* lds, int tid, int wv) {
;     const int lane = tid & 63;
;     const float* s = src + (size_t)(16 * wv) * ld_src + 4 * lane;
;     f32x4 va[16], vb[16];
;     cvt8_load(va, s, ld_src);
; #pragma unroll
;     for (int t = 0; t < 8; t += 2) {
;         cvt8_load(vb, s + (t + 1) * 256, ld_src); __builtin_amdgcn_sched_barrier(0);
; __device__ __forceinline__ void conv_queue(const Params& p, LAS unsigned char* lds, const int wave, const int cw, const int first, const int last, const int slot_off = LDS_MISC) {
;     ...
;     for (;;) {
;         __syncthreads();
;         if (tid == 0) *slot = first + (int)atomicAdd(&p.ctl[cw], 1u);
;         __syncthreads();
;         const int it = *slot;
;         if (it >= last) break;
;         if (it < N_GU) { const int e = it >> 5, rem = it & 31, kb = rem >> 1, nh = rem & 1;
;             const float* src = p.w_gu + (size_t)e * ND * (2 * DFF) + (size_t)(kb * 128) * (2 * DFF) + nh * 2048;
;             fp8_t* dst = p.wt_gu + (size_t)e * (2 * DFF) * ND + (size_t)(nh * 2048) * ND + kb * 128;
;             cvt_item_lds(src, 2 * DFF, dst, ND, lds, tid, wave); }
;         else { const int j = it - N_GU, e = j >> 4, kb = j & 15;
;             const float* src = p.w_down + (size_t)e * DFF * ND + (size_t)(kb * 128) * ND;
;             fp8_t* dst = p.wt_down + (size_t)e * ND * DFF + kb * 128;
;             cvt_item_lds(src, ND, dst, DFF, lds, tid, wave); }
.LBB0_822:
	s_or_b64 exec, exec, s[48:49]
	s_waitcnt lgkmcnt(0)
	s_barrier
	ds_read_b32 v0, v209
	s_movk_i32 s2, 0x3ff
	s_mov_b64 s[48:49], -1
	s_waitcnt lgkmcnt(0)
	v_cmp_lt_i32_e32 vcc, s2, v0
	v_readfirstlane_b32 s33, v0
	s_cbranch_vccnz .LBB0_817
	s_cmpk_gt_i32 s33, 0x3ff
	s_cbranch_scc0 .LBB0_825
	s_add_i32 s2, s33, 0xfffffc00
	s_lshr_b32 s4, s2, 4
	v_readlane_b32 s16, v254, 22
	s_lshl_b64 s[34:35], s[4:5], 22
	s_lshl_b64 s[48:49], s[4:5], 24
	v_readlane_b32 s20, v254, 26
	v_readlane_b32 s21, v254, 27
	s_add_u32 s2, s20, s48
	s_addc_u32 s4, s21, s49
	s_lshl_b32 s48, s33, 7
	s_and_b32 s48, s48, 0x780
	s_lshl_b32 s49, s48, 13
	s_add_u32 s2, s2, s49
	s_addc_u32 s4, s4, 0
	s_add_u32 s34, s56, s34
	s_addc_u32 s35, s57, s35
	s_add_u32 s50, s34, s48
	s_addc_u32 s51, s35, 0
	s_add_u32 s48, s2, s14
	s_addc_u32 s49, s4, s15
	v_lshl_add_u64 v[172:173], s[48:49], 0, v[128:129]
	s_movk_i32 s2, 0x2000
	v_add_co_u32_e32 v174, vcc, s2, v172
	s_movk_i32 s2, 0x3000
	s_nop 0
	v_addc_co_u32_e32 v175, vcc, 0, v173, vcc
	v_add_co_u32_e32 v142, vcc, s2, v172
	s_movk_i32 s2, 0x6000
	s_nop 0
	v_addc_co_u32_e32 v143, vcc, 0, v173, vcc
	v_add_co_u32_e32 v176, vcc, s13, v172
	v_readlane_b32 s17, v254, 23
	s_nop 0
	v_addc_co_u32_e32 v177, vcc, 0, v173, vcc
	v_add_co_u32_e32 v144, vcc, s67, v172
	v_readlane_b32 s18, v254, 24
	s_nop 0
	v_addc_co_u32_e32 v145, vcc, 0, v173, vcc
	v_add_co_u32_e32 v178, vcc, s2, v172
	s_movk_i32 s2, 0x7000
	s_nop 0
	v_addc_co_u32_e32 v179, vcc, 0, v173, vcc
	v_add_co_u32_e32 v146, vcc, s2, v172
	s_mov_b32 s2, 0xa000
	s_nop 0
	v_addc_co_u32_e32 v147, vcc, 0, v173, vcc
	v_add_co_u32_e32 v180, vcc, s60, v172
	global_load_dwordx4 v[16:19], v[144:145], off offset:-4096 nt
	global_load_dwordx4 v[20:23], v[146:147], off offset:-4096 nt
	v_addc_co_u32_e32 v181, vcc, 0, v173, vcc
	v_add_co_u32_e32 v148, vcc, s68, v172
	v_readlane_b32 s19, v254, 25
	s_nop 0
	v_addc_co_u32_e32 v149, vcc, 0, v173, vcc
	v_add_co_u32_e32 v182, vcc, s2, v172
	s_mov_b32 s2, 0xb000
	s_nop 0
	v_addc_co_u32_e32 v183, vcc, 0, v173, vcc
	v_add_co_u32_e32 v150, vcc, s2, v172
	s_mov_b32 s2, 0xe000
	s_nop 0
	v_addc_co_u32_e32 v151, vcc, 0, v173, vcc
	v_add_co_u32_e32 v184, vcc, s61, v172
	global_load_dwordx4 v[24:27], v[148:149], off offset:-4096 nt
	global_load_dwordx4 v[28:31], v[150:151], off offset:-4096 nt
	v_addc_co_u32_e32 v185, vcc, 0, v173, vcc
	v_add_co_u32_e32 v152, vcc, s69, v172
	v_readlane_b32 s22, v254, 28
	s_nop 0
	v_addc_co_u32_e32 v153, vcc, 0, v173, vcc
	v_add_co_u32_e32 v186, vcc, s2, v172
	s_mov_b32 s2, 0xf000
	s_nop 0
	v_addc_co_u32_e32 v187, vcc, 0, v173, vcc
	v_add_co_u32_e32 v154, vcc, s2, v172
	s_mov_b32 s2, 0x12000
	s_nop 0
	v_addc_co_u32_e32 v155, vcc, 0, v173, vcc
	v_add_co_u32_e32 v188, vcc, s62, v172
	global_load_dwordx4 v[56:59], v[152:153], off offset:-4096 nt
	global_load_dwordx4 v[60:63], v[154:155], off offset:-4096 nt
	v_addc_co_u32_e32 v189, vcc, 0, v173, vcc
	v_add_co_u32_e32 v156, vcc, s88, v172
	v_readlane_b32 s23, v254, 29
	s_nop 0
	v_addc_co_u32_e32 v157, vcc, 0, v173, vcc
	v_add_co_u32_e32 v190, vcc, s2, v172
	s_mov_b32 s2, 0x13000
	s_nop 0
	v_addc_co_u32_e32 v191, vcc, 0, v173, vcc
	v_add_co_u32_e32 v158, vcc, s2, v172
	s_mov_b32 s2, 0x16000
	s_nop 0
	v_addc_co_u32_e32 v159, vcc, 0, v173, vcc
	v_add_co_u32_e32 v192, vcc, s63, v172
	global_load_dwordx4 v[48:51], v[156:157], off offset:-4096 nt
	global_load_dwordx4 v[52:55], v[158:159], off offset:-4096 nt
	v_addc_co_u32_e32 v193, vcc, 0, v173, vcc
	v_add_co_u32_e32 v160, vcc, s89, v172
	v_readlane_b32 s24, v254, 30
	s_nop 0
	v_addc_co_u32_e32 v161, vcc, 0, v173, vcc
	v_add_co_u32_e32 v194, vcc, s2, v172
	s_mov_b32 s2, 0x17000
	s_nop 0
	v_addc_co_u32_e32 v195, vcc, 0, v173, vcc
	v_add_co_u32_e32 v162, vcc, s2, v172
	s_mov_b32 s2, 0x1a000
	s_nop 0
	v_addc_co_u32_e32 v163, vcc, 0, v173, vcc
	v_add_co_u32_e32 v196, vcc, s64, v172
	global_load_dwordx4 v[80:83], v[160:161], off offset:-4096 nt
	global_load_dwordx4 v[84:87], v[162:163], off offset:-4096 nt
	v_addc_co_u32_e32 v197, vcc, 0, v173, vcc
	v_add_co_u32_e32 v164, vcc, s90, v172
	v_readlane_b32 s25, v254, 31
	s_nop 0
	v_addc_co_u32_e32 v165, vcc, 0, v173, vcc
	v_add_co_u32_e32 v198, vcc, s2, v172
	s_mov_b32 s2, 0x1b000
	s_nop 0
	v_addc_co_u32_e32 v199, vcc, 0, v173, vcc
	v_add_co_u32_e32 v166, vcc, s2, v172
	s_mov_b32 s2, 0x1e000
	s_nop 0
	v_addc_co_u32_e32 v167, vcc, 0, v173, vcc
	v_add_co_u32_e32 v200, vcc, s65, v172
	global_load_dwordx4 v[88:91], v[164:165], off offset:-4096 nt
	global_load_dwordx4 v[92:95], v[166:167], off offset:-4096 nt
	v_addc_co_u32_e32 v201, vcc, 0, v173, vcc
	v_add_co_u32_e32 v168, vcc, s91, v172
	v_readlane_b32 s26, v254, 32
	s_nop 0
	v_addc_co_u32_e32 v169, vcc, 0, v173, vcc
	v_add_co_u32_e32 v202, vcc, s2, v172
	s_mov_b32 s2, 0x1f000
	s_nop 0
	v_addc_co_u32_e32 v203, vcc, 0, v173, vcc
	v_add_co_u32_e32 v170, vcc, s2, v172
	v_readlane_b32 s27, v254, 33
	s_nop 0
	v_addc_co_u32_e32 v171, vcc, 0, v173, vcc
	global_load_dwordx4 v[108:111], v[168:169], off offset:-4096 nt
	global_load_dwordx4 v[112:115], v[170:171], off offset:-4096 nt
	global_load_dwordx4 v[116:119], v[142:143], off offset:-4096 nt
	global_load_dwordx4 v[96:99], v128, s[48:49] offset:1024 nt
	global_load_dwordx4 v[100:103], v[174:175], off offset:1024 nt
	global_load_dwordx4 v[104:107], v[176:177], off offset:1024 nt
	global_load_dwordx4 v[124:127], v[178:179], off offset:1024 nt
	global_load_dwordx4 v[64:67], v[180:181], off offset:1024 nt
	global_load_dwordx4 v[68:71], v[182:183], off offset:1024 nt
	global_load_dwordx4 v[72:75], v[184:185], off offset:1024 nt
	global_load_dwordx4 v[76:79], v[186:187], off offset:1024 nt
	global_load_dwordx4 v[32:35], v[188:189], off offset:1024 nt
	global_load_dwordx4 v[36:39], v[190:191], off offset:1024 nt
	global_load_dwordx4 v[40:43], v[192:193], off offset:1024 nt
	global_load_dwordx4 v[44:47], v[194:195], off offset:1024 nt
	global_load_dwordx4 v[0:3], v[196:197], off offset:1024 nt
	global_load_dwordx4 v[4:7], v[198:199], off offset:1024 nt
	global_load_dwordx4 v[8:11], v[200:201], off offset:1024 nt
	global_load_dwordx4 v[120:123], v128, s[48:49] nt
	global_load_dwordx4 v[12:15], v[202:203], off offset:1024 nt
	v_readlane_b32 s28, v254, 34
	v_readlane_b32 s29, v254, 35
	v_readlane_b32 s30, v254, 36
	v_readlane_b32 s31, v254, 37
	v_lshl_add_u64 v[140:141], s[50:51], 0, v[130:131]
	s_waitcnt vmcnt(1)
; #define LAS __attribute__((address_space(3)))
; __device__ __forceinline__ unsigned pack4_fp8(float a, float b, float c, float d) { int r = 0; r = __builtin_amdgcn_cvt_pk_fp8_f32(a, b, r, false); r = __builtin_amdgcn_cvt_pk_fp8_f32(c, d, r, true); return (unsigned)r; }
; #define CVT_LDS_BAR() do { asm volatile("s_waitcnt lgkmcnt(0)" ::: "memory"); __builtin_amdgcn_s_barrier(); asm volatile("" ::: "memory"); } while (0)
; __device__ __forceinline__ void cvt8_to_lds(const f32x4 (&v)[16], LAS unsigned char* tile, int lane, int wv) {
; #pragma unroll
;     for (int i = 0; i < 4; ++i) { u32x4 w; w.x = pack4_fp8(v[0][i] * W8_SCALE, v[1][i] * W8_SCALE, v[2][i] * W8_SCALE, v[3][i] * W8_SCALE); w.y = pack4_fp8(v[4][i] * W8_SCALE, v[5][i] * W8_SCALE, v[6][i] * W8_SCALE, v[7][i] * W8_SCALE);
;         w.z = pack4_fp8(v[8][i] * W8_SCALE, v[9][i] * W8_SCALE, v[10][i] * W8_SCALE, v[11][i] * W8_SCALE); w.w = pack4_fp8(v[12][i] * W8_SCALE, v[13][i] * W8_SCALE, v[14][i] * W8_SCALE, v[15][i] * W8_SCALE);
;         *(LAS u32x4*)(tile + (4 * lane + i) * 128 + ((wv ^ (lane & 7)) << 4)) = w; }
; }
; __device__ __forceinline__ void cvt8_from_lds(const LAS unsigned char* tile, fp8_t* d, int ld_dst, int tid) {
;     const int c = tid & 7;
; #pragma unroll
;     for (int q = 0; q < 4; ++q) { const int r = (tid >> 3) + 64 * q; const u32x4 w = *(const LAS u32x4*)(tile + r * 128 + ((c ^ ((r >> 2) & 7)) << 4));
;         __builtin_nontemporal_store(w, (u32x4*)(d + (size_t)r * ld_dst + 16 * c)); }
; }
; __device__ __forceinline__ void cvt_item_lds(const float* src, int ld_src, fp8_t* dst, int ld_dst, LAS unsigned char* lds, int tid, int wv) {
;     const int lane = tid & 63;
;     const float* s = src + (size_t)(16 * wv) * ld_src + 4 * lane;
;     f32x4 va[16], vb[16];
;     cvt8_load(va, s, ld_src);
; #pragma unroll
;     for (int t = 0; t < 8; t += 2) {
;         cvt8_load(vb, s + (t + 1) * 256, ld_src); __builtin_amdgcn_sched_barrier(0);
;         cvt8_to_lds(va, lds, lane, wv); CVT_LDS_BAR(); __builtin_amdgcn_sched_barrier(0);
;         cvt8_from_lds(lds, dst + (size_t)(t * 256) * ld_dst, ld_dst, tid); __builtin_amdgcn_sched_barrier(0);
	v_mul_f32_e32 v120, 0x42800000, v120
	v_mul_f32_e32 v116, 0x42800000, v116
	v_mov_b32_e32 v210, v129
	v_cvt_pk_fp8_f32 v210, v120, v116
	v_mul_f32_e32 v16, 0x42800000, v16
	v_mul_f32_e32 v20, 0x42800000, v20
	v_mov_b32_e32 v211, v129
	v_cvt_pk_fp8_f32 v210, v16, v20 op_sel:[0,0,1]
	v_mul_f32_e32 v16, 0x42800000, v24
	v_mul_f32_e32 v20, 0x42800000, v28
	v_cvt_pk_fp8_f32 v211, v16, v20
	v_mul_f32_e32 v16, 0x42800000, v48
	v_mul_f32_e32 v20, 0x42800000, v52
	v_mov_b32_e32 v212, v129
	v_cvt_pk_fp8_f32 v212, v16, v20
	v_mul_f32_e32 v16, 0x42800000, v88
	v_mul_f32_e32 v20, 0x42800000, v92
	v_mov_b32_e32 v213, v129
	v_cvt_pk_fp8_f32 v213, v16, v20
	v_mul_f32_e32 v24, 0x42800000, v56
	v_mul_f32_e32 v28, 0x42800000, v60
	v_cvt_pk_fp8_f32 v211, v24, v28 op_sel:[0,0,1]
	v_mul_f32_e32 v24, 0x42800000, v80
	v_mul_f32_e32 v28, 0x42800000, v84
	v_cvt_pk_fp8_f32 v212, v24, v28 op_sel:[0,0,1]
	v_mul_f32_e32 v24, 0x42800000, v108
	v_mul_f32_e32 v28, 0x42800000, v112
	v_cvt_pk_fp8_f32 v213, v24, v28 op_sel:[0,0,1]
	v_mul_f32_e32 v16, 0x42800000, v121
	v_mul_f32_e32 v20, 0x42800000, v117
	v_mul_f32_e32 v17, 0x42800000, v17
	ds_write_b128 v204, v[210:213]
	v_mov_b32_e32 v210, v129
	v_cvt_pk_fp8_f32 v210, v16, v20
	v_mul_f32_e32 v21, 0x42800000, v21
	v_mul_f32_e32 v16, 0x42800000, v25
	v_mov_b32_e32 v211, v129
	v_cvt_pk_fp8_f32 v210, v17, v21 op_sel:[0,0,1]
	v_mul_f32_e32 v17, 0x42800000, v29
	v_cvt_pk_fp8_f32 v211, v16, v17
	v_mul_f32_e32 v16, 0x42800000, v49
	v_mul_f32_e32 v17, 0x42800000, v53
	v_mov_b32_e32 v212, v129
	v_cvt_pk_fp8_f32 v212, v16, v17
	v_mul_f32_e32 v16, 0x42800000, v89
	v_mul_f32_e32 v17, 0x42800000, v93
	v_mov_b32_e32 v213, v129
	v_cvt_pk_fp8_f32 v213, v16, v17
	v_mul_f32_e32 v20, 0x42800000, v57
	v_mul_f32_e32 v21, 0x42800000, v61
	v_cvt_pk_fp8_f32 v211, v20, v21 op_sel:[0,0,1]
	v_mul_f32_e32 v20, 0x42800000, v81
	v_mul_f32_e32 v21, 0x42800000, v85
	v_cvt_pk_fp8_f32 v212, v20, v21 op_sel:[0,0,1]
	v_mul_f32_e32 v20, 0x42800000, v109
	v_mul_f32_e32 v21, 0x42800000, v113
	v_cvt_pk_fp8_f32 v213, v20, v21 op_sel:[0,0,1]
	v_mul_f32_e32 v16, 0x42800000, v122
	v_mul_f32_e32 v17, 0x42800000, v118
	v_mul_f32_e32 v18, 0x42800000, v18
	ds_write_b128 v204, v[210:213] offset:128
	v_mov_b32_e32 v210, v129
	v_cvt_pk_fp8_f32 v210, v16, v17
	v_mul_f32_e32 v16, 0x42800000, v26
	v_mul_f32_e32 v17, 0x42800000, v30
	v_mov_b32_e32 v211, v129
	v_cvt_pk_fp8_f32 v211, v16, v17
	v_mul_f32_e32 v16, 0x42800000, v50
	v_mul_f32_e32 v17, 0x42800000, v54
	v_mov_b32_e32 v212, v129
	v_cvt_pk_fp8_f32 v212, v16, v17
	v_mul_f32_e32 v16, 0x42800000, v90
	v_mul_f32_e32 v17, 0x42800000, v94
	v_mov_b32_e32 v213, v129
	v_mul_f32_e32 v20, 0x42800000, v22
	v_cvt_pk_fp8_f32 v213, v16, v17
	v_cvt_pk_fp8_f32 v210, v18, v20 op_sel:[0,0,1]
	v_mul_f32_e32 v18, 0x42800000, v58
	v_mul_f32_e32 v20, 0x42800000, v62
	v_cvt_pk_fp8_f32 v211, v18, v20 op_sel:[0,0,1]
	v_mul_f32_e32 v18, 0x42800000, v82
	v_mul_f32_e32 v20, 0x42800000, v86
	v_cvt_pk_fp8_f32 v212, v18, v20 op_sel:[0,0,1]
	v_mul_f32_e32 v18, 0x42800000, v110
	v_mul_f32_e32 v20, 0x42800000, v114
	v_cvt_pk_fp8_f32 v213, v18, v20 op_sel:[0,0,1]
	v_mul_f32_e32 v17, 0x42800000, v123
	v_mul_f32_e32 v18, 0x42800000, v119
	v_mov_b32_e32 v16, v129
	v_cvt_pk_fp8_f32 v16, v17, v18
	v_mul_f32_e32 v19, 0x42800000, v19
	v_mul_f32_e32 v20, 0x42800000, v23
	v_mul_f32_e32 v18, 0x42800000, v27
	v_cvt_pk_fp8_f32 v16, v19, v20 op_sel:[0,0,1]
	v_mul_f32_e32 v19, 0x42800000, v31
	v_mov_b32_e32 v17, v129
	v_cvt_pk_fp8_f32 v17, v18, v19
	v_mul_f32_e32 v20, 0x42800000, v59
	v_mul_f32_e32 v21, 0x42800000, v63
	v_mul_f32_e32 v19, 0x42800000, v51
	v_cvt_pk_fp8_f32 v17, v20, v21 op_sel:[0,0,1]
	v_mul_f32_e32 v20, 0x42800000, v55
	v_mov_b32_e32 v18, v129
	v_cvt_pk_fp8_f32 v18, v19, v20
	v_mul_f32_e32 v21, 0x42800000, v83
	v_mul_f32_e32 v22, 0x42800000, v87
	v_mul_f32_e32 v20, 0x42800000, v91
	v_cvt_pk_fp8_f32 v18, v21, v22 op_sel:[0,0,1]
	v_mul_f32_e32 v21, 0x42800000, v95
	v_mov_b32_e32 v19, v129
	v_cvt_pk_fp8_f32 v19, v20, v21
	v_mul_f32_e32 v22, 0x42800000, v111
	v_mul_f32_e32 v23, 0x42800000, v115
	ds_write_b128 v204, v[210:213] offset:256
	v_cvt_pk_fp8_f32 v19, v22, v23 op_sel:[0,0,1]
	ds_write_b128 v204, v[16:19] offset:384
	s_waitcnt lgkmcnt(0)
	s_barrier
	ds_read_b128 v[16:19], v205
	v_lshl_add_u64 v[20:21], v[140:141], 0, v[132:133]
	s_waitcnt lgkmcnt(0)
	global_store_dwordx4 v[20:21], v[16:19], off nt
	ds_read_b128 v[16:19], v206
	v_lshl_add_u64 v[20:21], v[140:141], 0, v[134:135]
	s_waitcnt lgkmcnt(0)
	global_store_dwordx4 v[20:21], v[16:19], off nt
	ds_read_b128 v[16:19], v207
	v_lshl_add_u64 v[20:21], v[140:141], 0, v[136:137]
	s_waitcnt lgkmcnt(0)
	global_store_dwordx4 v[20:21], v[16:19], off nt
	ds_read_b128 v[16:19], v208
	v_lshl_add_u64 v[20:21], v[140:141], 0, v[138:139]
	s_waitcnt lgkmcnt(0)
; #define LAS __attribute__((address_space(3)))
; __device__ __forceinline__ unsigned pack4_fp8(float a, float b, float c, float d) { int r = 0; r = __builtin_amdgcn_cvt_pk_fp8_f32(a, b, r, false); r = __builtin_amdgcn_cvt_pk_fp8_f32(c, d, r, true); return (unsigned)r; }
; __device__ __forceinline__ void cvt8_to_lds(const f32x4 (&v)[16], LAS unsigned char* tile, int lane, int wv) {
; #pragma unroll
;     for (int i = 0; i < 4; ++i) { u32x4 w; w.x = pack4_fp8(v[0][i] * W8_SCALE, v[1][i] * W8_SCALE, v[2][i] * W8_SCALE, v[3][i] * W8_SCALE); w.y = pack4_fp8(v[4][i] * W8_SCALE, v[5][i] * W8_SCALE, v[6][i] * W8_SCALE, v[7][i] * W8_SCALE);
;         w.z = pack4_fp8(v[8][i] * W8_SCALE, v[9][i] * W8_SCALE, v[10][i] * W8_SCALE, v[11][i] * W8_SCALE); w.w = pack4_fp8(v[12][i] * W8_SCALE, v[13][i] * W8_SCALE, v[14][i] * W8_SCALE, v[15][i] * W8_SCALE);
;         *(LAS u32x4*)(tile + (4 * lane + i) * 128 + ((wv ^ (lane & 7)) << 4)) = w; }
; }
; __device__ __forceinline__ void cvt8_from_lds(const LAS unsigned char* tile, fp8_t* d, int ld_dst, int tid) {
;     const int c = tid & 7;
; #pragma unroll
;     for (int q = 0; q < 4; ++q) { const int r = (tid >> 3) + 64 * q; const u32x4 w = *(const LAS u32x4*)(tile + r * 128 + ((c ^ ((r >> 2) & 7)) << 4));
;         __builtin_nontemporal_store(w, (u32x4*)(d + (size_t)r * ld_dst + 16 * c)); }
; }
; __device__ __forceinline__ void cvt_item_lds(const float* src, int ld_src, fp8_t* dst, int ld_dst, LAS unsigned char* lds, int tid, int wv) {
;     const int lane = tid & 63;
;     const float* s = src + (size_t)(16 * wv) * ld_src + 4 * lane;
;     f32x4 va[16], vb[16];
;     cvt8_load(va, s, ld_src);
; #pragma unroll
;     for (int t = 0; t < 8; t += 2) {
;         cvt8_load(vb, s + (t + 1) * 256, ld_src); __builtin_amdgcn_sched_barrier(0);
;         cvt8_to_lds(va, lds, lane, wv); CVT_LDS_BAR(); __builtin_amdgcn_sched_barrier(0);
;         cvt8_from_lds(lds, dst + (size_t)(t * 256) * ld_dst, ld_dst, tid); __builtin_amdgcn_sched_barrier(0);
;         if (t + 2 < 8) { cvt8_load(va, s + (t + 2) * 256, ld_src); __builtin_amdgcn_sched_barrier(0); }
;         cvt8_to_lds(vb, lds + 32768, lane, wv); CVT_LDS_BAR(); __builtin_amdgcn_sched_barrier(0);
;         cvt8_from_lds(lds + 32768, dst + (size_t)((t + 1) * 256) * ld_dst, ld_dst, tid); __builtin_amdgcn_sched_barrier(0);
	global_store_dwordx4 v[20:21], v[16:19], off nt
	global_load_dwordx4 v[108:111], v[174:175], off offset:2048 nt
	global_load_dwordx4 v[112:115], v[176:177], off offset:2048 nt
	global_load_dwordx4 v[116:119], v[178:179], off offset:2048 nt
	global_load_dwordx4 v[80:83], v[180:181], off offset:2048 nt
	global_load_dwordx4 v[84:87], v[182:183], off offset:2048 nt
	global_load_dwordx4 v[88:91], v[184:185], off offset:2048 nt
	global_load_dwordx4 v[92:95], v[186:187], off offset:2048 nt
	global_load_dwordx4 v[48:51], v[188:189], off offset:2048 nt
	global_load_dwordx4 v[52:55], v[190:191], off offset:2048 nt
	global_load_dwordx4 v[56:59], v[192:193], off offset:2048 nt
	global_load_dwordx4 v[60:63], v[194:195], off offset:2048 nt
	global_load_dwordx4 v[16:19], v[196:197], off offset:2048 nt
	global_load_dwordx4 v[20:23], v[198:199], off offset:2048 nt
	global_load_dwordx4 v[24:27], v[200:201], off offset:2048 nt
	global_load_dwordx4 v[120:123], v128, s[48:49] offset:2048 nt
	global_load_dwordx4 v[28:31], v[202:203], off offset:2048 nt
	v_mul_f32_e32 v96, 0x42800000, v96
	v_mul_f32_e32 v100, 0x42800000, v100
	v_mov_b32_e32 v210, v129
	v_mul_f32_e32 v64, 0x42800000, v64
	v_mul_f32_e32 v68, 0x42800000, v68
	v_mov_b32_e32 v211, v129
	v_mul_f32_e32 v32, 0x42800000, v32
	v_mul_f32_e32 v36, 0x42800000, v36
	v_mov_b32_e32 v212, v129
	v_mul_f32_e32 v0, 0x42800000, v0
	v_mul_f32_e32 v4, 0x42800000, v4
	v_mov_b32_e32 v213, v129
	v_cvt_pk_fp8_f32 v210, v96, v100
	v_cvt_pk_fp8_f32 v211, v64, v68
	v_cvt_pk_fp8_f32 v212, v32, v36
	v_cvt_pk_fp8_f32 v213, v0, v4
	v_mul_f32_e32 v104, 0x42800000, v104
	v_mul_f32_e32 v124, 0x42800000, v124
	v_mul_f32_e32 v72, 0x42800000, v72
	v_mul_f32_e32 v76, 0x42800000, v76
	v_mul_f32_e32 v40, 0x42800000, v40
	v_mul_f32_e32 v44, 0x42800000, v44
	v_mul_f32_e32 v8, 0x42800000, v8
	s_waitcnt vmcnt(20)
	v_mul_f32_e32 v12, 0x42800000, v12
	v_cvt_pk_fp8_f32 v210, v104, v124 op_sel:[0,0,1]
	v_cvt_pk_fp8_f32 v211, v72, v76 op_sel:[0,0,1]
	v_cvt_pk_fp8_f32 v212, v40, v44 op_sel:[0,0,1]
	v_cvt_pk_fp8_f32 v213, v8, v12 op_sel:[0,0,1]
	v_mul_f32_e32 v0, 0x42800000, v97
	v_mul_f32_e32 v4, 0x42800000, v101
	v_mul_f32_e32 v8, 0x42800000, v105
	ds_write_b128 v204, v[210:213] offset:32768
	v_mov_b32_e32 v210, v129
	v_cvt_pk_fp8_f32 v210, v0, v4
	v_mul_f32_e32 v0, 0x42800000, v65
	v_mul_f32_e32 v4, 0x42800000, v69
	v_mov_b32_e32 v211, v129
	v_cvt_pk_fp8_f32 v211, v0, v4
	v_mul_f32_e32 v0, 0x42800000, v33
	v_mul_f32_e32 v4, 0x42800000, v37
	v_mov_b32_e32 v212, v129
	v_cvt_pk_fp8_f32 v212, v0, v4
	v_mul_f32_e32 v0, 0x42800000, v1
	v_mul_f32_e32 v1, 0x42800000, v5
	v_mov_b32_e32 v213, v129
	v_cvt_pk_fp8_f32 v213, v0, v1
	v_mul_f32_e32 v12, 0x42800000, v125
	v_cvt_pk_fp8_f32 v210, v8, v12 op_sel:[0,0,1]
	v_mul_f32_e32 v8, 0x42800000, v73
	v_mul_f32_e32 v12, 0x42800000, v77
	v_cvt_pk_fp8_f32 v211, v8, v12 op_sel:[0,0,1]
	v_mul_f32_e32 v8, 0x42800000, v41
	v_mul_f32_e32 v12, 0x42800000, v45
	v_mul_f32_e32 v4, 0x42800000, v9
	v_mul_f32_e32 v5, 0x42800000, v13
	v_cvt_pk_fp8_f32 v212, v8, v12 op_sel:[0,0,1]
	v_cvt_pk_fp8_f32 v213, v4, v5 op_sel:[0,0,1]
	v_mul_f32_e32 v0, 0x42800000, v98
	v_mul_f32_e32 v1, 0x42800000, v102
	v_mul_f32_e32 v4, 0x42800000, v106
	ds_write_b128 v204, v[210:213] offset:32896
	v_mov_b32_e32 v210, v129
	v_cvt_pk_fp8_f32 v210, v0, v1
	v_mul_f32_e32 v0, 0x42800000, v66
	v_mul_f32_e32 v1, 0x42800000, v70
	v_mov_b32_e32 v211, v129
	v_cvt_pk_fp8_f32 v211, v0, v1
	v_mul_f32_e32 v0, 0x42800000, v34
	v_mul_f32_e32 v1, 0x42800000, v38
	v_mov_b32_e32 v212, v129
	v_cvt_pk_fp8_f32 v212, v0, v1
	v_mul_f32_e32 v0, 0x42800000, v2
	v_mul_f32_e32 v1, 0x42800000, v6
	v_mov_b32_e32 v213, v129
	v_mul_f32_e32 v5, 0x42800000, v126
	v_cvt_pk_fp8_f32 v213, v0, v1
	v_cvt_pk_fp8_f32 v210, v4, v5 op_sel:[0,0,1]
	v_mul_f32_e32 v4, 0x42800000, v74
	v_mul_f32_e32 v5, 0x42800000, v78
	v_cvt_pk_fp8_f32 v211, v4, v5 op_sel:[0,0,1]
	v_mul_f32_e32 v4, 0x42800000, v42
	v_mul_f32_e32 v5, 0x42800000, v46
	v_cvt_pk_fp8_f32 v212, v4, v5 op_sel:[0,0,1]
	v_mul_f32_e32 v2, 0x42800000, v10
	v_mul_f32_e32 v4, 0x42800000, v14
	v_cvt_pk_fp8_f32 v213, v2, v4 op_sel:[0,0,1]
	v_mul_f32_e32 v1, 0x42800000, v99
	v_mul_f32_e32 v2, 0x42800000, v103
	v_mov_b32_e32 v0, v129
	v_cvt_pk_fp8_f32 v0, v1, v2
	v_mul_f32_e32 v4, 0x42800000, v107
	v_mul_f32_e32 v5, 0x42800000, v127
	v_mul_f32_e32 v2, 0x42800000, v67
	v_cvt_pk_fp8_f32 v0, v4, v5 op_sel:[0,0,1]
	v_mul_f32_e32 v4, 0x42800000, v71
	v_mov_b32_e32 v1, v129
	v_cvt_pk_fp8_f32 v1, v2, v4
	v_mul_f32_e32 v5, 0x42800000, v75
	v_mul_f32_e32 v6, 0x42800000, v79
	v_mul_f32_e32 v4, 0x42800000, v35
	v_cvt_pk_fp8_f32 v1, v5, v6 op_sel:[0,0,1]
	v_mul_f32_e32 v5, 0x42800000, v39
	v_mov_b32_e32 v2, v129
	v_cvt_pk_fp8_f32 v2, v4, v5
	v_mul_f32_e32 v4, 0x42800000, v3
	v_mul_f32_e32 v5, 0x42800000, v7
	v_mov_b32_e32 v3, v129
	v_cvt_pk_fp8_f32 v3, v4, v5
	v_mul_f32_e32 v6, 0x42800000, v43
	v_mul_f32_e32 v8, 0x42800000, v47
	v_cvt_pk_fp8_f32 v2, v6, v8 op_sel:[0,0,1]
	v_mul_f32_e32 v6, 0x42800000, v11
	v_mul_f32_e32 v7, 0x42800000, v15
	v_cvt_pk_fp8_f32 v3, v6, v7 op_sel:[0,0,1]
	ds_write_b128 v204, v[210:213] offset:33024
	ds_write_b128 v204, v[0:3] offset:33152
	s_waitcnt lgkmcnt(0)
	s_barrier
; #define LAS __attribute__((address_space(3)))
; __device__ __forceinline__ unsigned pack4_fp8(float a, float b, float c, float d) { int r = 0; r = __builtin_amdgcn_cvt_pk_fp8_f32(a, b, r, false); r = __builtin_amdgcn_cvt_pk_fp8_f32(c, d, r, true); return (unsigned)r; }
; __device__ __forceinline__ void cvt8_to_lds(const f32x4 (&v)[16], LAS unsigned char* tile, int lane, int wv) {
; #pragma unroll
;     for (int i = 0; i < 4; ++i) { u32x4 w; w.x = pack4_fp8(v[0][i] * W8_SCALE, v[1][i] * W8_SCALE, v[2][i] * W8_SCALE, v[3][i] * W8_SCALE); w.y = pack4_fp8(v[4][i] * W8_SCALE, v[5][i] * W8_SCALE, v[6][i] * W8_SCALE, v[7][i] * W8_SCALE);
;         w.z = pack4_fp8(v[8][i] * W8_SCALE, v[9][i] * W8_SCALE, v[10][i] * W8_SCALE, v[11][i] * W8_SCALE); w.w = pack4_fp8(v[12][i] * W8_SCALE, v[13][i] * W8_SCALE, v[14][i] * W8_SCALE, v[15][i] * W8_SCALE);
;         *(LAS u32x4*)(tile + (4 * lane + i) * 128 + ((wv ^ (lane & 7)) << 4)) = w; }
; }
; __device__ __forceinline__ void cvt8_from_lds(const LAS unsigned char* tile, fp8_t* d, int ld_dst, int tid) {
;     const int c = tid & 7;
; #pragma unroll
;     for (int q = 0; q < 4; ++q) { const int r = (tid >> 3) + 64 * q; const u32x4 w = *(const LAS u32x4*)(tile + r * 128 + ((c ^ ((r >> 2) & 7)) << 4));
;         __builtin_nontemporal_store(w, (u32x4*)(d + (size_t)r * ld_dst + 16 * c)); }
; }
; __device__ __forceinline__ void cvt_item_lds(const float* src, int ld_src, fp8_t* dst, int ld_dst, LAS unsigned char* lds, int tid, int wv) {
;     const int lane = tid & 63;
;     const float* s = src + (size_t)(16 * wv) * ld_src + 4 * lane;
;     f32x4 va[16], vb[16];
;     cvt8_load(va, s, ld_src);
; #pragma unroll
;     for (int t = 0; t < 8; t += 2) {
;         cvt8_load(vb, s + (t + 1) * 256, ld_src); __builtin_amdgcn_sched_barrier(0);
;         cvt8_to_lds(va, lds, lane, wv); CVT_LDS_BAR(); __builtin_amdgcn_sched_barrier(0);
;         cvt8_from_lds(lds, dst + (size_t)(t * 256) * ld_dst, ld_dst, tid); __builtin_amdgcn_sched_barrier(0);
;         if (t + 2 < 8) { cvt8_load(va, s + (t + 2) * 256, ld_src); __builtin_amdgcn_sched_barrier(0); }
;         cvt8_to_lds(vb, lds + 32768, lane, wv); CVT_LDS_BAR(); __builtin_amdgcn_sched_barrier(0);
;         cvt8_from_lds(lds + 32768, dst + (size_t)((t + 1) * 256) * ld_dst, ld_dst, tid); __builtin_amdgcn_sched_barrier(0);
	ds_read_b128 v[0:3], v205 offset:32768
	v_lshl_add_u64 v[4:5], v[140:141], 0, s[8:9]
	v_lshl_add_u64 v[6:7], v[4:5], 0, v[132:133]
	s_waitcnt lgkmcnt(0)
	global_store_dwordx4 v[6:7], v[0:3], off nt
	ds_read_b128 v[0:3], v206 offset:32768
	v_lshl_add_u64 v[6:7], v[4:5], 0, v[134:135]
	s_waitcnt lgkmcnt(0)
	global_store_dwordx4 v[6:7], v[0:3], off nt
	ds_read_b128 v[0:3], v207 offset:32768
	v_lshl_add_u64 v[6:7], v[4:5], 0, v[136:137]
	v_lshl_add_u64 v[4:5], v[4:5], 0, v[138:139]
	s_waitcnt lgkmcnt(0)
	global_store_dwordx4 v[6:7], v[0:3], off nt
	ds_read_b128 v[0:3], v208 offset:32768
	s_waitcnt lgkmcnt(0)
	global_store_dwordx4 v[4:5], v[0:3], off nt
	global_load_dwordx4 v[96:99], v[174:175], off offset:3072 nt
	global_load_dwordx4 v[100:103], v[176:177], off offset:3072 nt
	global_load_dwordx4 v[104:107], v[178:179], off offset:3072 nt
	global_load_dwordx4 v[64:67], v[180:181], off offset:3072 nt
	global_load_dwordx4 v[68:71], v[182:183], off offset:3072 nt
	global_load_dwordx4 v[72:75], v[184:185], off offset:3072 nt
	global_load_dwordx4 v[76:79], v[186:187], off offset:3072 nt
	global_load_dwordx4 v[32:35], v[188:189], off offset:3072 nt
	global_load_dwordx4 v[36:39], v[190:191], off offset:3072 nt
	global_load_dwordx4 v[40:43], v[192:193], off offset:3072 nt
	global_load_dwordx4 v[44:47], v[194:195], off offset:3072 nt
	global_load_dwordx4 v[0:3], v[196:197], off offset:3072 nt
	global_load_dwordx4 v[4:7], v[198:199], off offset:3072 nt
	global_load_dwordx4 v[8:11], v[200:201], off offset:3072 nt
	global_load_dwordx4 v[124:127], v128, s[48:49] offset:3072 nt
	global_load_dwordx4 v[12:15], v[202:203], off offset:3072 nt
	s_waitcnt vmcnt(21)
	v_mul_f32_e32 v120, 0x42800000, v120
	v_mul_f32_e32 v108, 0x42800000, v108
	v_mov_b32_e32 v174, v129
	v_mul_f32_e32 v80, 0x42800000, v80
	v_mul_f32_e32 v84, 0x42800000, v84
	v_mov_b32_e32 v175, v129
	v_mul_f32_e32 v48, 0x42800000, v48
	v_mul_f32_e32 v52, 0x42800000, v52
	v_mov_b32_e32 v176, v129
	v_mul_f32_e32 v16, 0x42800000, v16
	v_mul_f32_e32 v20, 0x42800000, v20
	v_mov_b32_e32 v177, v129
	v_cvt_pk_fp8_f32 v174, v120, v108
	v_cvt_pk_fp8_f32 v175, v80, v84
	v_cvt_pk_fp8_f32 v176, v48, v52
	v_cvt_pk_fp8_f32 v177, v16, v20
	v_mul_f32_e32 v112, 0x42800000, v112
	v_mul_f32_e32 v116, 0x42800000, v116
	v_mul_f32_e32 v88, 0x42800000, v88
	v_mul_f32_e32 v92, 0x42800000, v92
	v_mul_f32_e32 v56, 0x42800000, v56
	v_mul_f32_e32 v60, 0x42800000, v60
	v_mul_f32_e32 v24, 0x42800000, v24
	s_waitcnt vmcnt(20)
	v_mul_f32_e32 v28, 0x42800000, v28
	v_cvt_pk_fp8_f32 v174, v112, v116 op_sel:[0,0,1]
	v_cvt_pk_fp8_f32 v175, v88, v92 op_sel:[0,0,1]
	v_cvt_pk_fp8_f32 v176, v56, v60 op_sel:[0,0,1]
	v_cvt_pk_fp8_f32 v177, v24, v28 op_sel:[0,0,1]
	v_mul_f32_e32 v16, 0x42800000, v121
	v_mul_f32_e32 v20, 0x42800000, v109
	v_mul_f32_e32 v24, 0x42800000, v113
	ds_write_b128 v204, v[174:177]
	v_mov_b32_e32 v174, v129
	v_cvt_pk_fp8_f32 v174, v16, v20
	v_mul_f32_e32 v16, 0x42800000, v81
	v_mul_f32_e32 v20, 0x42800000, v85
	v_mov_b32_e32 v175, v129
	v_cvt_pk_fp8_f32 v175, v16, v20
	v_mul_f32_e32 v16, 0x42800000, v49
	v_mul_f32_e32 v20, 0x42800000, v53
	v_mov_b32_e32 v176, v129
	v_cvt_pk_fp8_f32 v176, v16, v20
	v_mul_f32_e32 v16, 0x42800000, v17
	v_mul_f32_e32 v17, 0x42800000, v21
	v_mov_b32_e32 v177, v129
	v_cvt_pk_fp8_f32 v177, v16, v17
	v_mul_f32_e32 v28, 0x42800000, v117
	v_cvt_pk_fp8_f32 v174, v24, v28 op_sel:[0,0,1]
	v_mul_f32_e32 v24, 0x42800000, v89
	v_mul_f32_e32 v28, 0x42800000, v93
	v_cvt_pk_fp8_f32 v175, v24, v28 op_sel:[0,0,1]
	v_mul_f32_e32 v24, 0x42800000, v57
	v_mul_f32_e32 v28, 0x42800000, v61
	v_mul_f32_e32 v20, 0x42800000, v25
	v_mul_f32_e32 v21, 0x42800000, v29
	v_cvt_pk_fp8_f32 v176, v24, v28 op_sel:[0,0,1]
	v_cvt_pk_fp8_f32 v177, v20, v21 op_sel:[0,0,1]
	v_mul_f32_e32 v16, 0x42800000, v122
	v_mul_f32_e32 v17, 0x42800000, v110
	v_mul_f32_e32 v20, 0x42800000, v114
	ds_write_b128 v204, v[174:177] offset:128
	v_mov_b32_e32 v174, v129
	v_cvt_pk_fp8_f32 v174, v16, v17
	v_mul_f32_e32 v16, 0x42800000, v82
	v_mul_f32_e32 v17, 0x42800000, v86
	v_mov_b32_e32 v175, v129
	v_cvt_pk_fp8_f32 v175, v16, v17
	v_mul_f32_e32 v16, 0x42800000, v50
	v_mul_f32_e32 v17, 0x42800000, v54
	v_mov_b32_e32 v176, v129
	v_cvt_pk_fp8_f32 v176, v16, v17
	v_mul_f32_e32 v16, 0x42800000, v18
	v_mul_f32_e32 v17, 0x42800000, v22
	v_mov_b32_e32 v177, v129
	v_mul_f32_e32 v21, 0x42800000, v118
	v_cvt_pk_fp8_f32 v177, v16, v17
	v_cvt_pk_fp8_f32 v174, v20, v21 op_sel:[0,0,1]
	v_mul_f32_e32 v20, 0x42800000, v90
	v_mul_f32_e32 v21, 0x42800000, v94
	v_cvt_pk_fp8_f32 v175, v20, v21 op_sel:[0,0,1]
	v_mul_f32_e32 v20, 0x42800000, v58
	v_mul_f32_e32 v21, 0x42800000, v62
	v_cvt_pk_fp8_f32 v176, v20, v21 op_sel:[0,0,1]
	v_mul_f32_e32 v18, 0x42800000, v26
	v_mul_f32_e32 v20, 0x42800000, v30
	v_cvt_pk_fp8_f32 v177, v18, v20 op_sel:[0,0,1]
	v_mul_f32_e32 v17, 0x42800000, v123
	v_mul_f32_e32 v18, 0x42800000, v111
	v_mov_b32_e32 v16, v129
	v_cvt_pk_fp8_f32 v16, v17, v18
	v_mul_f32_e32 v20, 0x42800000, v115
	v_mul_f32_e32 v21, 0x42800000, v119
	v_mul_f32_e32 v18, 0x42800000, v83
	v_cvt_pk_fp8_f32 v16, v20, v21 op_sel:[0,0,1]
	v_mul_f32_e32 v20, 0x42800000, v87
	v_mov_b32_e32 v17, v129
	v_cvt_pk_fp8_f32 v17, v18, v20
	v_mul_f32_e32 v21, 0x42800000, v91
	v_mul_f32_e32 v22, 0x42800000, v95
	v_mul_f32_e32 v20, 0x42800000, v51
	v_cvt_pk_fp8_f32 v17, v21, v22 op_sel:[0,0,1]
	v_mul_f32_e32 v21, 0x42800000, v55
	v_mov_b32_e32 v18, v129
	v_cvt_pk_fp8_f32 v18, v20, v21
	v_mul_f32_e32 v20, 0x42800000, v19
	v_mul_f32_e32 v21, 0x42800000, v23
	v_mov_b32_e32 v19, v129
	v_cvt_pk_fp8_f32 v19, v20, v21
	v_mul_f32_e32 v22, 0x42800000, v59
	v_mul_f32_e32 v24, 0x42800000, v63
	v_cvt_pk_fp8_f32 v18, v22, v24 op_sel:[0,0,1]
	v_mul_f32_e32 v22, 0x42800000, v27
	v_mul_f32_e32 v23, 0x42800000, v31
	v_cvt_pk_fp8_f32 v19, v22, v23 op_sel:[0,0,1]
	ds_write_b128 v204, v[174:177] offset:256
	ds_write_b128 v204, v[16:19] offset:384
	s_waitcnt lgkmcnt(0)
	s_barrier
; #define LAS __attribute__((address_space(3)))
; __device__ __forceinline__ unsigned pack4_fp8(float a, float b, float c, float d) { int r = 0; r = __builtin_amdgcn_cvt_pk_fp8_f32(a, b, r, false); r = __builtin_amdgcn_cvt_pk_fp8_f32(c, d, r, true); return (unsigned)r; }
; __device__ __forceinline__ void cvt8_to_lds(const f32x4 (&v)[16], LAS unsigned char* tile, int lane, int wv) {
; #pragma unroll
;     for (int i = 0; i < 4; ++i) { u32x4 w; w.x = pack4_fp8(v[0][i] * W8_SCALE, v[1][i] * W8_SCALE, v[2][i] * W8_SCALE, v[3][i] * W8_SCALE); w.y = pack4_fp8(v[4][i] * W8_SCALE, v[5][i] * W8_SCALE, v[6][i] * W8_SCALE, v[7][i] * W8_SCALE);
;         w.z = pack4_fp8(v[8][i] * W8_SCALE, v[9][i] * W8_SCALE, v[10][i] * W8_SCALE, v[11][i] * W8_SCALE); w.w = pack4_fp8(v[12][i] * W8_SCALE, v[13][i] * W8_SCALE, v[14][i] * W8_SCALE, v[15][i] * W8_SCALE);
;         *(LAS u32x4*)(tile + (4 * lane + i) * 128 + ((wv ^ (lane & 7)) << 4)) = w; }
; }
; __device__ __forceinline__ void cvt8_from_lds(const LAS unsigned char* tile, fp8_t* d, int ld_dst, int tid) {
;     const int c = tid & 7;
; #pragma unroll
;     for (int q = 0; q < 4; ++q) { const int r = (tid >> 3) + 64 * q; const u32x4 w = *(const LAS u32x4*)(tile + r * 128 + ((c ^ ((r >> 2) & 7)) << 4));
;         __builtin_nontemporal_store(w, (u32x4*)(d + (size_t)r * ld_dst + 16 * c)); }
; }
; __device__ __forceinline__ void cvt_item_lds(const float* src, int ld_src, fp8_t* dst, int ld_dst, LAS unsigned char* lds, int tid, int wv) {
;     const int lane = tid & 63;
;     const float* s = src + (size_t)(16 * wv) * ld_src + 4 * lane;
;     f32x4 va[16], vb[16];
;     cvt8_load(va, s, ld_src);
; #pragma unroll
;     for (int t = 0; t < 8; t += 2) {
;         cvt8_load(vb, s + (t + 1) * 256, ld_src); __builtin_amdgcn_sched_barrier(0);
;         cvt8_to_lds(va, lds, lane, wv); CVT_LDS_BAR(); __builtin_amdgcn_sched_barrier(0);
;         cvt8_from_lds(lds, dst + (size_t)(t * 256) * ld_dst, ld_dst, tid); __builtin_amdgcn_sched_barrier(0);
;         if (t + 2 < 8) { cvt8_load(va, s + (t + 2) * 256, ld_src); __builtin_amdgcn_sched_barrier(0); }
;         cvt8_to_lds(vb, lds + 32768, lane, wv); CVT_LDS_BAR(); __builtin_amdgcn_sched_barrier(0);
;         cvt8_from_lds(lds + 32768, dst + (size_t)((t + 1) * 256) * ld_dst, ld_dst, tid); __builtin_amdgcn_sched_barrier(0);
	ds_read_b128 v[16:19], v205
	v_lshl_add_u64 v[20:21], v[140:141], 0, s[10:11]
	v_lshl_add_u64 v[22:23], v[20:21], 0, v[132:133]
	s_waitcnt lgkmcnt(0)
	global_store_dwordx4 v[22:23], v[16:19], off nt
	ds_read_b128 v[16:19], v206
	v_lshl_add_u64 v[22:23], v[20:21], 0, v[134:135]
	s_waitcnt lgkmcnt(0)
	global_store_dwordx4 v[22:23], v[16:19], off nt
	ds_read_b128 v[16:19], v207
	v_lshl_add_u64 v[22:23], v[20:21], 0, v[136:137]
	v_lshl_add_u64 v[20:21], v[20:21], 0, v[138:139]
	s_waitcnt lgkmcnt(0)
	global_store_dwordx4 v[22:23], v[16:19], off nt
	ds_read_b128 v[16:19], v208
	s_waitcnt lgkmcnt(0)
	global_store_dwordx4 v[20:21], v[16:19], off nt
	v_add_co_u32_e32 v172, vcc, s66, v172
	s_nop 1
	v_addc_co_u32_e32 v173, vcc, 0, v173, vcc
	global_load_dwordx4 v[108:111], v[172:173], off nt
	global_load_dwordx4 v[112:115], v[142:143], off nt
	global_load_dwordx4 v[116:119], v[144:145], off nt
	global_load_dwordx4 v[120:123], v[146:147], off nt
	global_load_dwordx4 v[80:83], v[148:149], off nt
	global_load_dwordx4 v[84:87], v[150:151], off nt
	global_load_dwordx4 v[88:91], v[152:153], off nt
	global_load_dwordx4 v[92:95], v[154:155], off nt
	global_load_dwordx4 v[48:51], v[156:157], off nt
	global_load_dwordx4 v[52:55], v[158:159], off nt
	global_load_dwordx4 v[56:59], v[160:161], off nt
	global_load_dwordx4 v[60:63], v[162:163], off nt
	global_load_dwordx4 v[16:19], v[164:165], off nt
	global_load_dwordx4 v[20:23], v[166:167], off nt
	global_load_dwordx4 v[24:27], v[168:169], off nt
	global_load_dwordx4 v[28:31], v[170:171], off nt
	s_waitcnt vmcnt(21)
	v_mul_f32_e32 v124, 0x42800000, v124
	v_mul_f32_e32 v96, 0x42800000, v96
	v_mov_b32_e32 v174, v129
	v_mul_f32_e32 v64, 0x42800000, v64
	v_mul_f32_e32 v68, 0x42800000, v68
	v_mov_b32_e32 v175, v129
	v_mul_f32_e32 v32, 0x42800000, v32
	v_mul_f32_e32 v36, 0x42800000, v36
	v_mov_b32_e32 v176, v129
	v_mul_f32_e32 v0, 0x42800000, v0
	v_mul_f32_e32 v4, 0x42800000, v4
	v_mov_b32_e32 v177, v129
	v_cvt_pk_fp8_f32 v174, v124, v96
	v_cvt_pk_fp8_f32 v175, v64, v68
	v_cvt_pk_fp8_f32 v176, v32, v36
	v_cvt_pk_fp8_f32 v177, v0, v4
	v_mul_f32_e32 v100, 0x42800000, v100
	v_mul_f32_e32 v104, 0x42800000, v104
	v_mul_f32_e32 v72, 0x42800000, v72
	v_mul_f32_e32 v76, 0x42800000, v76
	v_mul_f32_e32 v40, 0x42800000, v40
	v_mul_f32_e32 v44, 0x42800000, v44
	v_mul_f32_e32 v8, 0x42800000, v8
	s_waitcnt vmcnt(20)
	v_mul_f32_e32 v12, 0x42800000, v12
	v_cvt_pk_fp8_f32 v174, v100, v104 op_sel:[0,0,1]
	v_cvt_pk_fp8_f32 v175, v72, v76 op_sel:[0,0,1]
	v_cvt_pk_fp8_f32 v176, v40, v44 op_sel:[0,0,1]
	v_cvt_pk_fp8_f32 v177, v8, v12 op_sel:[0,0,1]
	v_mul_f32_e32 v0, 0x42800000, v125
	v_mul_f32_e32 v4, 0x42800000, v97
	v_mul_f32_e32 v8, 0x42800000, v101
	ds_write_b128 v204, v[174:177] offset:32768
	v_mov_b32_e32 v174, v129
	v_cvt_pk_fp8_f32 v174, v0, v4
	v_mul_f32_e32 v0, 0x42800000, v65
	v_mul_f32_e32 v4, 0x42800000, v69
	v_mov_b32_e32 v175, v129
	v_cvt_pk_fp8_f32 v175, v0, v4
	v_mul_f32_e32 v0, 0x42800000, v33
	v_mul_f32_e32 v4, 0x42800000, v37
	v_mov_b32_e32 v176, v129
	v_cvt_pk_fp8_f32 v176, v0, v4
	v_mul_f32_e32 v0, 0x42800000, v1
	v_mul_f32_e32 v1, 0x42800000, v5
	v_mov_b32_e32 v177, v129
	v_cvt_pk_fp8_f32 v177, v0, v1
	v_mul_f32_e32 v12, 0x42800000, v105
	v_cvt_pk_fp8_f32 v174, v8, v12 op_sel:[0,0,1]
	v_mul_f32_e32 v8, 0x42800000, v73
	v_mul_f32_e32 v12, 0x42800000, v77
	v_cvt_pk_fp8_f32 v175, v8, v12 op_sel:[0,0,1]
	v_mul_f32_e32 v8, 0x42800000, v41
	v_mul_f32_e32 v12, 0x42800000, v45
	v_mul_f32_e32 v4, 0x42800000, v9
	v_mul_f32_e32 v5, 0x42800000, v13
	v_cvt_pk_fp8_f32 v176, v8, v12 op_sel:[0,0,1]
	v_cvt_pk_fp8_f32 v177, v4, v5 op_sel:[0,0,1]
	v_mul_f32_e32 v0, 0x42800000, v126
	v_mul_f32_e32 v1, 0x42800000, v98
	v_mul_f32_e32 v4, 0x42800000, v102
	ds_write_b128 v204, v[174:177] offset:32896
	v_mov_b32_e32 v174, v129
	v_cvt_pk_fp8_f32 v174, v0, v1
	v_mul_f32_e32 v0, 0x42800000, v66
	v_mul_f32_e32 v1, 0x42800000, v70
	v_mov_b32_e32 v175, v129
	v_cvt_pk_fp8_f32 v175, v0, v1
	v_mul_f32_e32 v0, 0x42800000, v34
	v_mul_f32_e32 v1, 0x42800000, v38
	v_mov_b32_e32 v176, v129
	v_cvt_pk_fp8_f32 v176, v0, v1
	v_mul_f32_e32 v0, 0x42800000, v2
	v_mul_f32_e32 v1, 0x42800000, v6
	v_mov_b32_e32 v177, v129
	v_mul_f32_e32 v5, 0x42800000, v106
	v_cvt_pk_fp8_f32 v177, v0, v1
	v_cvt_pk_fp8_f32 v174, v4, v5 op_sel:[0,0,1]
	v_mul_f32_e32 v4, 0x42800000, v74
	v_mul_f32_e32 v5, 0x42800000, v78
	v_cvt_pk_fp8_f32 v175, v4, v5 op_sel:[0,0,1]
	v_mul_f32_e32 v4, 0x42800000, v42
	v_mul_f32_e32 v5, 0x42800000, v46
	v_cvt_pk_fp8_f32 v176, v4, v5 op_sel:[0,0,1]
	v_mul_f32_e32 v2, 0x42800000, v10
	v_mul_f32_e32 v4, 0x42800000, v14
	v_cvt_pk_fp8_f32 v177, v2, v4 op_sel:[0,0,1]
	v_mul_f32_e32 v1, 0x42800000, v127
	v_mul_f32_e32 v2, 0x42800000, v99
	v_mov_b32_e32 v0, v129
	v_cvt_pk_fp8_f32 v0, v1, v2
	v_mul_f32_e32 v4, 0x42800000, v103
	v_mul_f32_e32 v5, 0x42800000, v107
	v_mul_f32_e32 v2, 0x42800000, v67
	v_cvt_pk_fp8_f32 v0, v4, v5 op_sel:[0,0,1]
	v_mul_f32_e32 v4, 0x42800000, v71
	v_mov_b32_e32 v1, v129
	v_cvt_pk_fp8_f32 v1, v2, v4
	v_mul_f32_e32 v5, 0x42800000, v75
	v_mul_f32_e32 v6, 0x42800000, v79
	v_mul_f32_e32 v4, 0x42800000, v35
	v_cvt_pk_fp8_f32 v1, v5, v6 op_sel:[0,0,1]
	v_mul_f32_e32 v5, 0x42800000, v39
	v_mov_b32_e32 v2, v129
	v_cvt_pk_fp8_f32 v2, v4, v5
	v_mul_f32_e32 v4, 0x42800000, v3
	v_mul_f32_e32 v5, 0x42800000, v7
	v_mov_b32_e32 v3, v129
	v_cvt_pk_fp8_f32 v3, v4, v5
	v_mul_f32_e32 v6, 0x42800000, v43
	v_mul_f32_e32 v8, 0x42800000, v47
	v_cvt_pk_fp8_f32 v2, v6, v8 op_sel:[0,0,1]
	v_mul_f32_e32 v6, 0x42800000, v11
	v_mul_f32_e32 v7, 0x42800000, v15
	v_cvt_pk_fp8_f32 v3, v6, v7 op_sel:[0,0,1]
	ds_write_b128 v204, v[174:177] offset:33024
	ds_write_b128 v204, v[0:3] offset:33152
	s_waitcnt lgkmcnt(0)
	s_barrier
; #define LAS __attribute__((address_space(3)))
; __device__ __forceinline__ unsigned pack4_fp8(float a, float b, float c, float d) { int r = 0; r = __builtin_amdgcn_cvt_pk_fp8_f32(a, b, r, false); r = __builtin_amdgcn_cvt_pk_fp8_f32(c, d, r, true); return (unsigned)r; }
; __device__ __forceinline__ void cvt8_to_lds(const f32x4 (&v)[16], LAS unsigned char* tile, int lane, int wv) {
; #pragma unroll
;     for (int i = 0; i < 4; ++i) { u32x4 w; w.x = pack4_fp8(v[0][i] * W8_SCALE, v[1][i] * W8_SCALE, v[2][i] * W8_SCALE, v[3][i] * W8_SCALE); w.y = pack4_fp8(v[4][i] * W8_SCALE, v[5][i] * W8_SCALE, v[6][i] * W8_SCALE, v[7][i] * W8_SCALE);
;         w.z = pack4_fp8(v[8][i] * W8_SCALE, v[9][i] * W8_SCALE, v[10][i] * W8_SCALE, v[11][i] * W8_SCALE); w.w = pack4_fp8(v[12][i] * W8_SCALE, v[13][i] * W8_SCALE, v[14][i] * W8_SCALE, v[15][i] * W8_SCALE);
;         *(LAS u32x4*)(tile + (4 * lane + i) * 128 + ((wv ^ (lane & 7)) << 4)) = w; }
; }
; __device__ __forceinline__ void cvt8_from_lds(const LAS unsigned char* tile, fp8_t* d, int ld_dst, int tid) {
;     const int c = tid & 7;
; #pragma unroll
;     for (int q = 0; q < 4; ++q) { const int r = (tid >> 3) + 64 * q; const u32x4 w = *(const LAS u32x4*)(tile + r * 128 + ((c ^ ((r >> 2) & 7)) << 4));
;         __builtin_nontemporal_store(w, (u32x4*)(d + (size_t)r * ld_dst + 16 * c)); }
; }
; __device__ __forceinline__ void cvt_item_lds(const float* src, int ld_src, fp8_t* dst, int ld_dst, LAS unsigned char* lds, int tid, int wv) {
;     const int lane = tid & 63;
;     const float* s = src + (size_t)(16 * wv) * ld_src + 4 * lane;
;     f32x4 va[16], vb[16];
;     cvt8_load(va, s, ld_src);
; #pragma unroll
;     for (int t = 0; t < 8; t += 2) {
;         cvt8_load(vb, s + (t + 1) * 256, ld_src); __builtin_amdgcn_sched_barrier(0);
;         cvt8_to_lds(va, lds, lane, wv); CVT_LDS_BAR(); __builtin_amdgcn_sched_barrier(0);
;         cvt8_from_lds(lds, dst + (size_t)(t * 256) * ld_dst, ld_dst, tid); __builtin_amdgcn_sched_barrier(0);
;         if (t + 2 < 8) { cvt8_load(va, s + (t + 2) * 256, ld_src); __builtin_amdgcn_sched_barrier(0); }
;         cvt8_to_lds(vb, lds + 32768, lane, wv); CVT_LDS_BAR(); __builtin_amdgcn_sched_barrier(0);
;         cvt8_from_lds(lds + 32768, dst + (size_t)((t + 1) * 256) * ld_dst, ld_dst, tid); __builtin_amdgcn_sched_barrier(0);
	ds_read_b128 v[0:3], v205 offset:32768
	v_lshl_add_u64 v[4:5], v[140:141], 0, s[38:39]
	v_lshl_add_u64 v[6:7], v[4:5], 0, v[132:133]
	s_waitcnt lgkmcnt(0)
	global_store_dwordx4 v[6:7], v[0:3], off nt
	ds_read_b128 v[0:3], v206 offset:32768
	v_lshl_add_u64 v[6:7], v[4:5], 0, v[134:135]
	s_waitcnt lgkmcnt(0)
	global_store_dwordx4 v[6:7], v[0:3], off nt
	ds_read_b128 v[0:3], v207 offset:32768
	v_lshl_add_u64 v[6:7], v[4:5], 0, v[136:137]
	v_lshl_add_u64 v[4:5], v[4:5], 0, v[138:139]
	s_waitcnt lgkmcnt(0)
	global_store_dwordx4 v[6:7], v[0:3], off nt
	ds_read_b128 v[0:3], v208 offset:32768
	s_waitcnt lgkmcnt(0)
	global_store_dwordx4 v[4:5], v[0:3], off nt
	global_load_dwordx4 v[96:99], v[172:173], off offset:1024 nt
	global_load_dwordx4 v[100:103], v[142:143], off offset:1024 nt
	global_load_dwordx4 v[104:107], v[144:145], off offset:1024 nt
	global_load_dwordx4 v[124:127], v[146:147], off offset:1024 nt
	global_load_dwordx4 v[64:67], v[148:149], off offset:1024 nt
	global_load_dwordx4 v[68:71], v[150:151], off offset:1024 nt
	global_load_dwordx4 v[72:75], v[152:153], off offset:1024 nt
	global_load_dwordx4 v[76:79], v[154:155], off offset:1024 nt
	global_load_dwordx4 v[32:35], v[156:157], off offset:1024 nt
	global_load_dwordx4 v[36:39], v[158:159], off offset:1024 nt
	global_load_dwordx4 v[40:43], v[160:161], off offset:1024 nt
	global_load_dwordx4 v[44:47], v[162:163], off offset:1024 nt
	global_load_dwordx4 v[0:3], v[164:165], off offset:1024 nt
	global_load_dwordx4 v[4:7], v[166:167], off offset:1024 nt
	global_load_dwordx4 v[8:11], v[168:169], off offset:1024 nt
	global_load_dwordx4 v[12:15], v[170:171], off offset:1024 nt
	s_waitcnt vmcnt(35)
	v_mul_f32_e32 v108, 0x42800000, v108
	s_waitcnt vmcnt(34)
	v_mul_f32_e32 v112, 0x42800000, v112
	v_mov_b32_e32 v174, v129
	s_waitcnt vmcnt(31)
	v_mul_f32_e32 v80, 0x42800000, v80
	s_waitcnt vmcnt(30)
	v_mul_f32_e32 v84, 0x42800000, v84
	v_mov_b32_e32 v175, v129
	s_waitcnt vmcnt(27)
	v_mul_f32_e32 v48, 0x42800000, v48
	s_waitcnt vmcnt(26)
	v_mul_f32_e32 v52, 0x42800000, v52
	v_mov_b32_e32 v176, v129
	s_waitcnt vmcnt(23)
	v_mul_f32_e32 v16, 0x42800000, v16
	s_waitcnt vmcnt(22)
	v_mul_f32_e32 v20, 0x42800000, v20
	v_mov_b32_e32 v177, v129
	v_cvt_pk_fp8_f32 v174, v108, v112
	v_cvt_pk_fp8_f32 v175, v80, v84
	v_cvt_pk_fp8_f32 v176, v48, v52
	v_cvt_pk_fp8_f32 v177, v16, v20
	v_mul_f32_e32 v116, 0x42800000, v116
	v_mul_f32_e32 v120, 0x42800000, v120
	v_mul_f32_e32 v88, 0x42800000, v88
	v_mul_f32_e32 v92, 0x42800000, v92
	v_mul_f32_e32 v56, 0x42800000, v56
	v_mul_f32_e32 v60, 0x42800000, v60
	s_waitcnt vmcnt(21)
	v_mul_f32_e32 v24, 0x42800000, v24
	s_waitcnt vmcnt(20)
	v_mul_f32_e32 v28, 0x42800000, v28
	v_cvt_pk_fp8_f32 v174, v116, v120 op_sel:[0,0,1]
	v_cvt_pk_fp8_f32 v175, v88, v92 op_sel:[0,0,1]
	v_cvt_pk_fp8_f32 v176, v56, v60 op_sel:[0,0,1]
	v_cvt_pk_fp8_f32 v177, v24, v28 op_sel:[0,0,1]
	v_mul_f32_e32 v16, 0x42800000, v109
	v_mul_f32_e32 v20, 0x42800000, v113
	v_mul_f32_e32 v24, 0x42800000, v117
	ds_write_b128 v204, v[174:177]
	v_mov_b32_e32 v174, v129
	v_cvt_pk_fp8_f32 v174, v16, v20
	v_mul_f32_e32 v16, 0x42800000, v81
	v_mul_f32_e32 v20, 0x42800000, v85
	v_mov_b32_e32 v175, v129
	v_cvt_pk_fp8_f32 v175, v16, v20
	v_mul_f32_e32 v16, 0x42800000, v49
	v_mul_f32_e32 v20, 0x42800000, v53
	v_mov_b32_e32 v176, v129
	v_cvt_pk_fp8_f32 v176, v16, v20
	v_mul_f32_e32 v16, 0x42800000, v17
	v_mul_f32_e32 v17, 0x42800000, v21
	v_mov_b32_e32 v177, v129
	v_cvt_pk_fp8_f32 v177, v16, v17
	v_mul_f32_e32 v28, 0x42800000, v121
	v_cvt_pk_fp8_f32 v174, v24, v28 op_sel:[0,0,1]
	v_mul_f32_e32 v24, 0x42800000, v89
	v_mul_f32_e32 v28, 0x42800000, v93
	v_cvt_pk_fp8_f32 v175, v24, v28 op_sel:[0,0,1]
	v_mul_f32_e32 v24, 0x42800000, v57
	v_mul_f32_e32 v28, 0x42800000, v61
	v_mul_f32_e32 v20, 0x42800000, v25
	v_mul_f32_e32 v21, 0x42800000, v29
	v_cvt_pk_fp8_f32 v176, v24, v28 op_sel:[0,0,1]
	v_cvt_pk_fp8_f32 v177, v20, v21 op_sel:[0,0,1]
	v_mul_f32_e32 v16, 0x42800000, v110
	v_mul_f32_e32 v17, 0x42800000, v114
	v_mul_f32_e32 v20, 0x42800000, v118
	ds_write_b128 v204, v[174:177] offset:128
	v_mov_b32_e32 v174, v129
	v_cvt_pk_fp8_f32 v174, v16, v17
	v_mul_f32_e32 v16, 0x42800000, v82
	v_mul_f32_e32 v17, 0x42800000, v86
	v_mov_b32_e32 v175, v129
	v_cvt_pk_fp8_f32 v175, v16, v17
	v_mul_f32_e32 v16, 0x42800000, v50
	v_mul_f32_e32 v17, 0x42800000, v54
	v_mov_b32_e32 v176, v129
	v_cvt_pk_fp8_f32 v176, v16, v17
	v_mul_f32_e32 v16, 0x42800000, v18
	v_mul_f32_e32 v17, 0x42800000, v22
	v_mov_b32_e32 v177, v129
	v_mul_f32_e32 v21, 0x42800000, v122
	v_cvt_pk_fp8_f32 v177, v16, v17
	v_cvt_pk_fp8_f32 v174, v20, v21 op_sel:[0,0,1]
	v_mul_f32_e32 v20, 0x42800000, v90
	v_mul_f32_e32 v21, 0x42800000, v94
	v_cvt_pk_fp8_f32 v175, v20, v21 op_sel:[0,0,1]
	v_mul_f32_e32 v20, 0x42800000, v58
	v_mul_f32_e32 v21, 0x42800000, v62
	v_cvt_pk_fp8_f32 v176, v20, v21 op_sel:[0,0,1]
	v_mul_f32_e32 v18, 0x42800000, v26
	v_mul_f32_e32 v20, 0x42800000, v30
	v_cvt_pk_fp8_f32 v177, v18, v20 op_sel:[0,0,1]
	v_mul_f32_e32 v17, 0x42800000, v111
	v_mul_f32_e32 v18, 0x42800000, v115
	v_mov_b32_e32 v16, v129
	v_cvt_pk_fp8_f32 v16, v17, v18
	v_mul_f32_e32 v20, 0x42800000, v119
	v_mul_f32_e32 v21, 0x42800000, v123
	v_mul_f32_e32 v18, 0x42800000, v83
	v_cvt_pk_fp8_f32 v16, v20, v21 op_sel:[0,0,1]
	v_mul_f32_e32 v20, 0x42800000, v87
	v_mov_b32_e32 v17, v129
	v_cvt_pk_fp8_f32 v17, v18, v20
	v_mul_f32_e32 v21, 0x42800000, v91
	v_mul_f32_e32 v22, 0x42800000, v95
	v_mul_f32_e32 v20, 0x42800000, v51
	v_cvt_pk_fp8_f32 v17, v21, v22 op_sel:[0,0,1]
	v_mul_f32_e32 v21, 0x42800000, v55
	v_mov_b32_e32 v18, v129
	v_cvt_pk_fp8_f32 v18, v20, v21
	v_mul_f32_e32 v20, 0x42800000, v19
	v_mul_f32_e32 v21, 0x42800000, v23
	v_mov_b32_e32 v19, v129
	v_cvt_pk_fp8_f32 v19, v20, v21
	v_mul_f32_e32 v22, 0x42800000, v59
	v_mul_f32_e32 v24, 0x42800000, v63
	v_cvt_pk_fp8_f32 v18, v22, v24 op_sel:[0,0,1]
	v_mul_f32_e32 v22, 0x42800000, v27
	v_mul_f32_e32 v23, 0x42800000, v31
	v_cvt_pk_fp8_f32 v19, v22, v23 op_sel:[0,0,1]
	ds_write_b128 v204, v[174:177] offset:256
	ds_write_b128 v204, v[16:19] offset:384
	s_waitcnt lgkmcnt(0)
	s_barrier
; #define LAS __attribute__((address_space(3)))
; __device__ __forceinline__ unsigned pack4_fp8(float a, float b, float c, float d) { int r = 0; r = __builtin_amdgcn_cvt_pk_fp8_f32(a, b, r, false); r = __builtin_amdgcn_cvt_pk_fp8_f32(c, d, r, true); return (unsigned)r; }
; __device__ __forceinline__ void cvt8_to_lds(const f32x4 (&v)[16], LAS unsigned char* tile, int lane, int wv) {
; #pragma unroll
;     for (int i = 0; i < 4; ++i) { u32x4 w; w.x = pack4_fp8(v[0][i] * W8_SCALE, v[1][i] * W8_SCALE, v[2][i] * W8_SCALE, v[3][i] * W8_SCALE); w.y = pack4_fp8(v[4][i] * W8_SCALE, v[5][i] * W8_SCALE, v[6][i] * W8_SCALE, v[7][i] * W8_SCALE);
;         w.z = pack4_fp8(v[8][i] * W8_SCALE, v[9][i] * W8_SCALE, v[10][i] * W8_SCALE, v[11][i] * W8_SCALE); w.w = pack4_fp8(v[12][i] * W8_SCALE, v[13][i] * W8_SCALE, v[14][i] * W8_SCALE, v[15][i] * W8_SCALE);
;         *(LAS u32x4*)(tile + (4 * lane + i) * 128 + ((wv ^ (lane & 7)) << 4)) = w; }
; }
; __device__ __forceinline__ void cvt8_from_lds(const LAS unsigned char* tile, fp8_t* d, int ld_dst, int tid) {
;     const int c = tid & 7;
; #pragma unroll
;     for (int q = 0; q < 4; ++q) { const int r = (tid >> 3) + 64 * q; const u32x4 w = *(const LAS u32x4*)(tile + r * 128 + ((c ^ ((r >> 2) & 7)) << 4));
;         __builtin_nontemporal_store(w, (u32x4*)(d + (size_t)r * ld_dst + 16 * c)); }
; }
; __device__ __forceinline__ void cvt_item_lds(const float* src, int ld_src, fp8_t* dst, int ld_dst, LAS unsigned char* lds, int tid, int wv) {
;     const int lane = tid & 63;
;     const float* s = src + (size_t)(16 * wv) * ld_src + 4 * lane;
;     f32x4 va[16], vb[16];
;     cvt8_load(va, s, ld_src);
; #pragma unroll
;     for (int t = 0; t < 8; t += 2) {
;         cvt8_load(vb, s + (t + 1) * 256, ld_src); __builtin_amdgcn_sched_barrier(0);
;         cvt8_to_lds(va, lds, lane, wv); CVT_LDS_BAR(); __builtin_amdgcn_sched_barrier(0);
;         cvt8_from_lds(lds, dst + (size_t)(t * 256) * ld_dst, ld_dst, tid); __builtin_amdgcn_sched_barrier(0);
;         if (t + 2 < 8) { cvt8_load(va, s + (t + 2) * 256, ld_src); __builtin_amdgcn_sched_barrier(0); }
;         cvt8_to_lds(vb, lds + 32768, lane, wv); CVT_LDS_BAR(); __builtin_amdgcn_sched_barrier(0);
;         cvt8_from_lds(lds + 32768, dst + (size_t)((t + 1) * 256) * ld_dst, ld_dst, tid); __builtin_amdgcn_sched_barrier(0);
	ds_read_b128 v[16:19], v205
	v_lshl_add_u64 v[20:21], v[140:141], 0, s[40:41]
	v_lshl_add_u64 v[22:23], v[20:21], 0, v[132:133]
	s_waitcnt lgkmcnt(0)
	global_store_dwordx4 v[22:23], v[16:19], off nt
	ds_read_b128 v[16:19], v206
	v_lshl_add_u64 v[22:23], v[20:21], 0, v[134:135]
	s_waitcnt lgkmcnt(0)
	global_store_dwordx4 v[22:23], v[16:19], off nt
	ds_read_b128 v[16:19], v207
	v_lshl_add_u64 v[22:23], v[20:21], 0, v[136:137]
	v_lshl_add_u64 v[20:21], v[20:21], 0, v[138:139]
	s_waitcnt lgkmcnt(0)
	global_store_dwordx4 v[22:23], v[16:19], off nt
	ds_read_b128 v[16:19], v208
	s_waitcnt lgkmcnt(0)
	global_store_dwordx4 v[20:21], v[16:19], off nt
	global_load_dwordx4 v[108:111], v[172:173], off offset:2048 nt
	global_load_dwordx4 v[112:115], v[142:143], off offset:2048 nt
	global_load_dwordx4 v[116:119], v[144:145], off offset:2048 nt
	global_load_dwordx4 v[120:123], v[146:147], off offset:2048 nt
	global_load_dwordx4 v[80:83], v[148:149], off offset:2048 nt
	global_load_dwordx4 v[84:87], v[150:151], off offset:2048 nt
	global_load_dwordx4 v[88:91], v[152:153], off offset:2048 nt
	global_load_dwordx4 v[92:95], v[154:155], off offset:2048 nt
	global_load_dwordx4 v[48:51], v[156:157], off offset:2048 nt
	global_load_dwordx4 v[52:55], v[158:159], off offset:2048 nt
	global_load_dwordx4 v[56:59], v[160:161], off offset:2048 nt
	global_load_dwordx4 v[60:63], v[162:163], off offset:2048 nt
	global_load_dwordx4 v[16:19], v[164:165], off offset:2048 nt
	global_load_dwordx4 v[20:23], v[166:167], off offset:2048 nt
	global_load_dwordx4 v[24:27], v[168:169], off offset:2048 nt
	global_load_dwordx4 v[28:31], v[170:171], off offset:2048 nt
	s_waitcnt vmcnt(35)
	v_mul_f32_e32 v96, 0x42800000, v96
	s_waitcnt vmcnt(34)
	v_mul_f32_e32 v100, 0x42800000, v100
	v_mov_b32_e32 v174, v129
	s_waitcnt vmcnt(31)
	v_mul_f32_e32 v64, 0x42800000, v64
	s_waitcnt vmcnt(30)
	v_mul_f32_e32 v68, 0x42800000, v68
	v_mov_b32_e32 v175, v129
	s_waitcnt vmcnt(27)
	v_mul_f32_e32 v32, 0x42800000, v32
	s_waitcnt vmcnt(26)
	v_mul_f32_e32 v36, 0x42800000, v36
	v_mov_b32_e32 v176, v129
	s_waitcnt vmcnt(23)
	v_mul_f32_e32 v0, 0x42800000, v0
	s_waitcnt vmcnt(22)
	v_mul_f32_e32 v4, 0x42800000, v4
	v_mov_b32_e32 v177, v129
	v_cvt_pk_fp8_f32 v174, v96, v100
	v_cvt_pk_fp8_f32 v175, v64, v68
	v_cvt_pk_fp8_f32 v176, v32, v36
	v_cvt_pk_fp8_f32 v177, v0, v4
	v_mul_f32_e32 v104, 0x42800000, v104
	v_mul_f32_e32 v124, 0x42800000, v124
	v_mul_f32_e32 v72, 0x42800000, v72
	v_mul_f32_e32 v76, 0x42800000, v76
	v_mul_f32_e32 v40, 0x42800000, v40
	v_mul_f32_e32 v44, 0x42800000, v44
	s_waitcnt vmcnt(21)
	v_mul_f32_e32 v8, 0x42800000, v8
	s_waitcnt vmcnt(20)
	v_mul_f32_e32 v12, 0x42800000, v12
	v_cvt_pk_fp8_f32 v174, v104, v124 op_sel:[0,0,1]
	v_cvt_pk_fp8_f32 v175, v72, v76 op_sel:[0,0,1]
	v_cvt_pk_fp8_f32 v176, v40, v44 op_sel:[0,0,1]
	v_cvt_pk_fp8_f32 v177, v8, v12 op_sel:[0,0,1]
	v_mul_f32_e32 v0, 0x42800000, v97
	v_mul_f32_e32 v4, 0x42800000, v101
	v_mul_f32_e32 v8, 0x42800000, v105
	ds_write_b128 v204, v[174:177] offset:32768
	v_mov_b32_e32 v174, v129
	v_cvt_pk_fp8_f32 v174, v0, v4
	v_mul_f32_e32 v0, 0x42800000, v65
	v_mul_f32_e32 v4, 0x42800000, v69
	v_mov_b32_e32 v175, v129
	v_cvt_pk_fp8_f32 v175, v0, v4
	v_mul_f32_e32 v0, 0x42800000, v33
	v_mul_f32_e32 v4, 0x42800000, v37
	v_mov_b32_e32 v176, v129
	v_cvt_pk_fp8_f32 v176, v0, v4
	v_mul_f32_e32 v0, 0x42800000, v1
	v_mul_f32_e32 v1, 0x42800000, v5
	v_mov_b32_e32 v177, v129
	v_cvt_pk_fp8_f32 v177, v0, v1
	v_mul_f32_e32 v12, 0x42800000, v125
	v_cvt_pk_fp8_f32 v174, v8, v12 op_sel:[0,0,1]
	v_mul_f32_e32 v8, 0x42800000, v73
	v_mul_f32_e32 v12, 0x42800000, v77
	v_cvt_pk_fp8_f32 v175, v8, v12 op_sel:[0,0,1]
	v_mul_f32_e32 v8, 0x42800000, v41
	v_mul_f32_e32 v12, 0x42800000, v45
	v_mul_f32_e32 v4, 0x42800000, v9
	v_mul_f32_e32 v5, 0x42800000, v13
	v_cvt_pk_fp8_f32 v176, v8, v12 op_sel:[0,0,1]
	v_cvt_pk_fp8_f32 v177, v4, v5 op_sel:[0,0,1]
	v_mul_f32_e32 v0, 0x42800000, v98
	v_mul_f32_e32 v1, 0x42800000, v102
	v_mul_f32_e32 v4, 0x42800000, v106
	ds_write_b128 v204, v[174:177] offset:32896
	v_mov_b32_e32 v174, v129
	v_cvt_pk_fp8_f32 v174, v0, v1
	v_mul_f32_e32 v0, 0x42800000, v66
	v_mul_f32_e32 v1, 0x42800000, v70
	v_mov_b32_e32 v175, v129
	v_cvt_pk_fp8_f32 v175, v0, v1
	v_mul_f32_e32 v0, 0x42800000, v34
	v_mul_f32_e32 v1, 0x42800000, v38
	v_mov_b32_e32 v176, v129
	v_cvt_pk_fp8_f32 v176, v0, v1
	v_mul_f32_e32 v0, 0x42800000, v2
	v_mul_f32_e32 v1, 0x42800000, v6
	v_mov_b32_e32 v177, v129
	v_mul_f32_e32 v5, 0x42800000, v126
	v_cvt_pk_fp8_f32 v177, v0, v1
	v_cvt_pk_fp8_f32 v174, v4, v5 op_sel:[0,0,1]
	v_mul_f32_e32 v4, 0x42800000, v74
	v_mul_f32_e32 v5, 0x42800000, v78
	v_cvt_pk_fp8_f32 v175, v4, v5 op_sel:[0,0,1]
	v_mul_f32_e32 v4, 0x42800000, v42
	v_mul_f32_e32 v5, 0x42800000, v46
	v_cvt_pk_fp8_f32 v176, v4, v5 op_sel:[0,0,1]
	v_mul_f32_e32 v2, 0x42800000, v10
	v_mul_f32_e32 v4, 0x42800000, v14
	v_cvt_pk_fp8_f32 v177, v2, v4 op_sel:[0,0,1]
	v_mul_f32_e32 v1, 0x42800000, v99
	v_mul_f32_e32 v2, 0x42800000, v103
	v_mov_b32_e32 v0, v129
	v_cvt_pk_fp8_f32 v0, v1, v2
	v_mul_f32_e32 v4, 0x42800000, v107
	v_mul_f32_e32 v5, 0x42800000, v127
	v_mul_f32_e32 v2, 0x42800000, v67
	v_cvt_pk_fp8_f32 v0, v4, v5 op_sel:[0,0,1]
	v_mul_f32_e32 v4, 0x42800000, v71
	v_mov_b32_e32 v1, v129
	v_cvt_pk_fp8_f32 v1, v2, v4
	v_mul_f32_e32 v5, 0x42800000, v75
	v_mul_f32_e32 v6, 0x42800000, v79
	v_mul_f32_e32 v4, 0x42800000, v35
	v_cvt_pk_fp8_f32 v1, v5, v6 op_sel:[0,0,1]
	v_mul_f32_e32 v5, 0x42800000, v39
	v_mov_b32_e32 v2, v129
	v_cvt_pk_fp8_f32 v2, v4, v5
	v_mul_f32_e32 v4, 0x42800000, v3
	v_mul_f32_e32 v5, 0x42800000, v7
	v_mov_b32_e32 v3, v129
	v_cvt_pk_fp8_f32 v3, v4, v5
	v_mul_f32_e32 v6, 0x42800000, v43
	v_mul_f32_e32 v8, 0x42800000, v47
	v_cvt_pk_fp8_f32 v2, v6, v8 op_sel:[0,0,1]
	v_mul_f32_e32 v6, 0x42800000, v11
	v_mul_f32_e32 v7, 0x42800000, v15
	v_cvt_pk_fp8_f32 v3, v6, v7 op_sel:[0,0,1]
	ds_write_b128 v204, v[174:177] offset:33024
	ds_write_b128 v204, v[0:3] offset:33152
	s_waitcnt lgkmcnt(0)
	s_barrier
; #define LAS __attribute__((address_space(3)))
; __device__ __forceinline__ unsigned pack4_fp8(float a, float b, float c, float d) { int r = 0; r = __builtin_amdgcn_cvt_pk_fp8_f32(a, b, r, false); r = __builtin_amdgcn_cvt_pk_fp8_f32(c, d, r, true); return (unsigned)r; }
; __device__ __forceinline__ void cvt8_to_lds(const f32x4 (&v)[16], LAS unsigned char* tile, int lane, int wv) {
; #pragma unroll
;     for (int i = 0; i < 4; ++i) { u32x4 w; w.x = pack4_fp8(v[0][i] * W8_SCALE, v[1][i] * W8_SCALE, v[2][i] * W8_SCALE, v[3][i] * W8_SCALE); w.y = pack4_fp8(v[4][i] * W8_SCALE, v[5][i] * W8_SCALE, v[6][i] * W8_SCALE, v[7][i] * W8_SCALE);
;         w.z = pack4_fp8(v[8][i] * W8_SCALE, v[9][i] * W8_SCALE, v[10][i] * W8_SCALE, v[11][i] * W8_SCALE); w.w = pack4_fp8(v[12][i] * W8_SCALE, v[13][i] * W8_SCALE, v[14][i] * W8_SCALE, v[15][i] * W8_SCALE);
;         *(LAS u32x4*)(tile + (4 * lane + i) * 128 + ((wv ^ (lane & 7)) << 4)) = w; }
; }
; __device__ __forceinline__ void cvt8_from_lds(const LAS unsigned char* tile, fp8_t* d, int ld_dst, int tid) {
;     const int c = tid & 7;
; #pragma unroll
;     for (int q = 0; q < 4; ++q) { const int r = (tid >> 3) + 64 * q; const u32x4 w = *(const LAS u32x4*)(tile + r * 128 + ((c ^ ((r >> 2) & 7)) << 4));
;         __builtin_nontemporal_store(w, (u32x4*)(d + (size_t)r * ld_dst + 16 * c)); }
; }
; __device__ __forceinline__ void cvt_item_lds(const float* src, int ld_src, fp8_t* dst, int ld_dst, LAS unsigned char* lds, int tid, int wv) {
;     const int lane = tid & 63;
;     const float* s = src + (size_t)(16 * wv) * ld_src + 4 * lane;
;     f32x4 va[16], vb[16];
;     cvt8_load(va, s, ld_src);
; #pragma unroll
;     for (int t = 0; t < 8; t += 2) {
;         cvt8_load(vb, s + (t + 1) * 256, ld_src); __builtin_amdgcn_sched_barrier(0);
;         cvt8_to_lds(va, lds, lane, wv); CVT_LDS_BAR(); __builtin_amdgcn_sched_barrier(0);
;         cvt8_from_lds(lds, dst + (size_t)(t * 256) * ld_dst, ld_dst, tid); __builtin_amdgcn_sched_barrier(0);
;         if (t + 2 < 8) { cvt8_load(va, s + (t + 2) * 256, ld_src); __builtin_amdgcn_sched_barrier(0); }
;         cvt8_to_lds(vb, lds + 32768, lane, wv); CVT_LDS_BAR(); __builtin_amdgcn_sched_barrier(0);
;         cvt8_from_lds(lds + 32768, dst + (size_t)((t + 1) * 256) * ld_dst, ld_dst, tid); __builtin_amdgcn_sched_barrier(0);
	ds_read_b128 v[0:3], v205 offset:32768
	v_lshl_add_u64 v[4:5], v[140:141], 0, s[42:43]
	v_lshl_add_u64 v[6:7], v[4:5], 0, v[132:133]
	s_waitcnt lgkmcnt(0)
	global_store_dwordx4 v[6:7], v[0:3], off nt
	ds_read_b128 v[0:3], v206 offset:32768
	v_lshl_add_u64 v[6:7], v[4:5], 0, v[134:135]
	s_waitcnt lgkmcnt(0)
	global_store_dwordx4 v[6:7], v[0:3], off nt
	ds_read_b128 v[0:3], v207 offset:32768
	v_lshl_add_u64 v[6:7], v[4:5], 0, v[136:137]
	v_lshl_add_u64 v[4:5], v[4:5], 0, v[138:139]
	s_waitcnt lgkmcnt(0)
	global_store_dwordx4 v[6:7], v[0:3], off nt
	ds_read_b128 v[0:3], v208 offset:32768
	s_waitcnt lgkmcnt(0)
	global_store_dwordx4 v[4:5], v[0:3], off nt
	global_load_dwordx4 v[96:99], v[172:173], off offset:3072 nt
	global_load_dwordx4 v[100:103], v[142:143], off offset:3072 nt
	global_load_dwordx4 v[104:107], v[144:145], off offset:3072 nt
	global_load_dwordx4 v[124:127], v[146:147], off offset:3072 nt
	global_load_dwordx4 v[64:67], v[148:149], off offset:3072 nt
	global_load_dwordx4 v[68:71], v[150:151], off offset:3072 nt
	global_load_dwordx4 v[72:75], v[152:153], off offset:3072 nt
	global_load_dwordx4 v[76:79], v[154:155], off offset:3072 nt
	global_load_dwordx4 v[32:35], v[156:157], off offset:3072 nt
	global_load_dwordx4 v[36:39], v[158:159], off offset:3072 nt
	global_load_dwordx4 v[40:43], v[160:161], off offset:3072 nt
	global_load_dwordx4 v[44:47], v[162:163], off offset:3072 nt
	global_load_dwordx4 v[0:3], v[164:165], off offset:3072 nt
	global_load_dwordx4 v[4:7], v[166:167], off offset:3072 nt
	global_load_dwordx4 v[8:11], v[168:169], off offset:3072 nt
	global_load_dwordx4 v[12:15], v[170:171], off offset:3072 nt
	s_waitcnt vmcnt(35)
	v_mul_f32_e32 v108, 0x42800000, v108
	s_waitcnt vmcnt(34)
	v_mul_f32_e32 v112, 0x42800000, v112
	v_mov_b32_e32 v142, v129
	s_waitcnt vmcnt(31)
	v_mul_f32_e32 v80, 0x42800000, v80
	s_waitcnt vmcnt(30)
	v_mul_f32_e32 v84, 0x42800000, v84
	v_mov_b32_e32 v143, v129
	s_waitcnt vmcnt(27)
	v_mul_f32_e32 v48, 0x42800000, v48
	s_waitcnt vmcnt(26)
	v_mul_f32_e32 v52, 0x42800000, v52
	v_mov_b32_e32 v144, v129
	s_waitcnt vmcnt(23)
	v_mul_f32_e32 v16, 0x42800000, v16
	s_waitcnt vmcnt(22)
	v_mul_f32_e32 v20, 0x42800000, v20
	v_mov_b32_e32 v145, v129
	v_cvt_pk_fp8_f32 v142, v108, v112
	v_cvt_pk_fp8_f32 v143, v80, v84
	v_cvt_pk_fp8_f32 v144, v48, v52
	v_cvt_pk_fp8_f32 v145, v16, v20
	v_mul_f32_e32 v116, 0x42800000, v116
	v_mul_f32_e32 v120, 0x42800000, v120
	v_mul_f32_e32 v88, 0x42800000, v88
	v_mul_f32_e32 v92, 0x42800000, v92
	v_mul_f32_e32 v56, 0x42800000, v56
	v_mul_f32_e32 v60, 0x42800000, v60
	s_waitcnt vmcnt(21)
	v_mul_f32_e32 v24, 0x42800000, v24
	s_waitcnt vmcnt(20)
	v_mul_f32_e32 v28, 0x42800000, v28
	v_cvt_pk_fp8_f32 v142, v116, v120 op_sel:[0,0,1]
	v_cvt_pk_fp8_f32 v143, v88, v92 op_sel:[0,0,1]
	v_cvt_pk_fp8_f32 v144, v56, v60 op_sel:[0,0,1]
	v_cvt_pk_fp8_f32 v145, v24, v28 op_sel:[0,0,1]
	v_mul_f32_e32 v16, 0x42800000, v109
	v_mul_f32_e32 v20, 0x42800000, v113
	v_mul_f32_e32 v24, 0x42800000, v117
	ds_write_b128 v204, v[142:145]
	v_mov_b32_e32 v142, v129
	v_cvt_pk_fp8_f32 v142, v16, v20
	v_mul_f32_e32 v16, 0x42800000, v81
	v_mul_f32_e32 v20, 0x42800000, v85
	v_mov_b32_e32 v143, v129
	v_cvt_pk_fp8_f32 v143, v16, v20
	v_mul_f32_e32 v16, 0x42800000, v49
	v_mul_f32_e32 v20, 0x42800000, v53
	v_mov_b32_e32 v144, v129
	v_cvt_pk_fp8_f32 v144, v16, v20
	v_mul_f32_e32 v16, 0x42800000, v17
	v_mul_f32_e32 v17, 0x42800000, v21
	v_mov_b32_e32 v145, v129
	v_cvt_pk_fp8_f32 v145, v16, v17
	v_mul_f32_e32 v28, 0x42800000, v121
	v_cvt_pk_fp8_f32 v142, v24, v28 op_sel:[0,0,1]
	v_mul_f32_e32 v24, 0x42800000, v89
	v_mul_f32_e32 v28, 0x42800000, v93
	v_cvt_pk_fp8_f32 v143, v24, v28 op_sel:[0,0,1]
	v_mul_f32_e32 v24, 0x42800000, v57
	v_mul_f32_e32 v28, 0x42800000, v61
	v_mul_f32_e32 v20, 0x42800000, v25
	v_mul_f32_e32 v21, 0x42800000, v29
	v_cvt_pk_fp8_f32 v144, v24, v28 op_sel:[0,0,1]
	v_cvt_pk_fp8_f32 v145, v20, v21 op_sel:[0,0,1]
	v_mul_f32_e32 v16, 0x42800000, v110
	v_mul_f32_e32 v17, 0x42800000, v114
	v_mul_f32_e32 v20, 0x42800000, v118
	ds_write_b128 v204, v[142:145] offset:128
	v_mov_b32_e32 v142, v129
	v_cvt_pk_fp8_f32 v142, v16, v17
	v_mul_f32_e32 v16, 0x42800000, v82
	v_mul_f32_e32 v17, 0x42800000, v86
	v_mov_b32_e32 v143, v129
	v_cvt_pk_fp8_f32 v143, v16, v17
	v_mul_f32_e32 v16, 0x42800000, v50
	v_mul_f32_e32 v17, 0x42800000, v54
	v_mov_b32_e32 v144, v129
	v_cvt_pk_fp8_f32 v144, v16, v17
	v_mul_f32_e32 v16, 0x42800000, v18
	v_mul_f32_e32 v17, 0x42800000, v22
	v_mov_b32_e32 v145, v129
	v_mul_f32_e32 v21, 0x42800000, v122
	v_cvt_pk_fp8_f32 v145, v16, v17
	v_cvt_pk_fp8_f32 v142, v20, v21 op_sel:[0,0,1]
	v_mul_f32_e32 v20, 0x42800000, v90
	v_mul_f32_e32 v21, 0x42800000, v94
	v_cvt_pk_fp8_f32 v143, v20, v21 op_sel:[0,0,1]
	v_mul_f32_e32 v20, 0x42800000, v58
	v_mul_f32_e32 v21, 0x42800000, v62
	v_cvt_pk_fp8_f32 v144, v20, v21 op_sel:[0,0,1]
	v_mul_f32_e32 v18, 0x42800000, v26
	v_mul_f32_e32 v20, 0x42800000, v30
	v_cvt_pk_fp8_f32 v145, v18, v20 op_sel:[0,0,1]
	v_mul_f32_e32 v17, 0x42800000, v111
	v_mul_f32_e32 v18, 0x42800000, v115
	v_mov_b32_e32 v16, v129
	v_cvt_pk_fp8_f32 v16, v17, v18
	v_mul_f32_e32 v20, 0x42800000, v119
	v_mul_f32_e32 v21, 0x42800000, v123
	v_mul_f32_e32 v18, 0x42800000, v83
	v_cvt_pk_fp8_f32 v16, v20, v21 op_sel:[0,0,1]
	v_mul_f32_e32 v20, 0x42800000, v87
	v_mov_b32_e32 v17, v129
	v_cvt_pk_fp8_f32 v17, v18, v20
	v_mul_f32_e32 v21, 0x42800000, v91
	v_mul_f32_e32 v22, 0x42800000, v95
	v_mul_f32_e32 v20, 0x42800000, v51
	v_cvt_pk_fp8_f32 v17, v21, v22 op_sel:[0,0,1]
	v_mul_f32_e32 v21, 0x42800000, v55
	v_mov_b32_e32 v18, v129
	v_cvt_pk_fp8_f32 v18, v20, v21
	v_mul_f32_e32 v20, 0x42800000, v19
	v_mul_f32_e32 v21, 0x42800000, v23
	v_mov_b32_e32 v19, v129
	v_cvt_pk_fp8_f32 v19, v20, v21
	v_mul_f32_e32 v22, 0x42800000, v59
	v_mul_f32_e32 v24, 0x42800000, v63
	v_cvt_pk_fp8_f32 v18, v22, v24 op_sel:[0,0,1]
	v_mul_f32_e32 v22, 0x42800000, v27
	v_mul_f32_e32 v23, 0x42800000, v31
	v_cvt_pk_fp8_f32 v19, v22, v23 op_sel:[0,0,1]
	ds_write_b128 v204, v[142:145] offset:256
	ds_write_b128 v204, v[16:19] offset:384
	s_waitcnt lgkmcnt(0)
	s_barrier
; #define LAS __attribute__((address_space(3)))
; __device__ __forceinline__ unsigned pack4_fp8(float a, float b, float c, float d) { int r = 0; r = __builtin_amdgcn_cvt_pk_fp8_f32(a, b, r, false); r = __builtin_amdgcn_cvt_pk_fp8_f32(c, d, r, true); return (unsigned)r; }
; __device__ __forceinline__ void cvt8_to_lds(const f32x4 (&v)[16], LAS unsigned char* tile, int lane, int wv) {
; #pragma unroll
;     for (int i = 0; i < 4; ++i) { u32x4 w; w.x = pack4_fp8(v[0][i] * W8_SCALE, v[1][i] * W8_SCALE, v[2][i] * W8_SCALE, v[3][i] * W8_SCALE); w.y = pack4_fp8(v[4][i] * W8_SCALE, v[5][i] * W8_SCALE, v[6][i] * W8_SCALE, v[7][i] * W8_SCALE);
;         w.z = pack4_fp8(v[8][i] * W8_SCALE, v[9][i] * W8_SCALE, v[10][i] * W8_SCALE, v[11][i] * W8_SCALE); w.w = pack4_fp8(v[12][i] * W8_SCALE, v[13][i] * W8_SCALE, v[14][i] * W8_SCALE, v[15][i] * W8_SCALE);
;         *(LAS u32x4*)(tile + (4 * lane + i) * 128 + ((wv ^ (lane & 7)) << 4)) = w; }
; }
; __device__ __forceinline__ void cvt8_from_lds(const LAS unsigned char* tile, fp8_t* d, int ld_dst, int tid) {
;     const int c = tid & 7;
; #pragma unroll
;     for (int q = 0; q < 4; ++q) { const int r = (tid >> 3) + 64 * q; const u32x4 w = *(const LAS u32x4*)(tile + r * 128 + ((c ^ ((r >> 2) & 7)) << 4));
;         __builtin_nontemporal_store(w, (u32x4*)(d + (size_t)r * ld_dst + 16 * c)); }
; }
; __device__ __forceinline__ void cvt_item_lds(const float* src, int ld_src, fp8_t* dst, int ld_dst, LAS unsigned char* lds, int tid, int wv) {
;     const int lane = tid & 63;
;     const float* s = src + (size_t)(16 * wv) * ld_src + 4 * lane;
;     f32x4 va[16], vb[16];
;     cvt8_load(va, s, ld_src);
; #pragma unroll
;     for (int t = 0; t < 8; t += 2) {
;         cvt8_load(vb, s + (t + 1) * 256, ld_src); __builtin_amdgcn_sched_barrier(0);
;         cvt8_to_lds(va, lds, lane, wv); CVT_LDS_BAR(); __builtin_amdgcn_sched_barrier(0);
;         cvt8_from_lds(lds, dst + (size_t)(t * 256) * ld_dst, ld_dst, tid); __builtin_amdgcn_sched_barrier(0);
;         if (t + 2 < 8) { cvt8_load(va, s + (t + 2) * 256, ld_src); __builtin_amdgcn_sched_barrier(0); }
;         cvt8_to_lds(vb, lds + 32768, lane, wv); CVT_LDS_BAR(); __builtin_amdgcn_sched_barrier(0);
;         cvt8_from_lds(lds + 32768, dst + (size_t)((t + 1) * 256) * ld_dst, ld_dst, tid); __builtin_amdgcn_sched_barrier(0);
;     }
	ds_read_b128 v[16:19], v205
	v_lshl_add_u64 v[20:21], v[140:141], 0, s[44:45]
	v_lshl_add_u64 v[22:23], v[20:21], 0, v[132:133]
	s_waitcnt lgkmcnt(0)
	global_store_dwordx4 v[22:23], v[16:19], off nt
	ds_read_b128 v[16:19], v206
	v_lshl_add_u64 v[22:23], v[20:21], 0, v[134:135]
	s_waitcnt lgkmcnt(0)
	global_store_dwordx4 v[22:23], v[16:19], off nt
	ds_read_b128 v[16:19], v207
	v_lshl_add_u64 v[22:23], v[20:21], 0, v[136:137]
	v_lshl_add_u64 v[20:21], v[20:21], 0, v[138:139]
	s_waitcnt lgkmcnt(0)
	global_store_dwordx4 v[22:23], v[16:19], off nt
	ds_read_b128 v[16:19], v208
	s_waitcnt lgkmcnt(0)
	global_store_dwordx4 v[20:21], v[16:19], off nt
	s_waitcnt vmcnt(19)
	s_nop 0
	v_mul_f32_e32 v17, 0x42800000, v96
	s_waitcnt vmcnt(18)
	v_mul_f32_e32 v18, 0x42800000, v100
	v_mov_b32_e32 v16, v129
	v_cvt_pk_fp8_f32 v16, v17, v18
	s_waitcnt vmcnt(17)
	v_mul_f32_e32 v19, 0x42800000, v104
	s_waitcnt vmcnt(16)
	v_mul_f32_e32 v20, 0x42800000, v124
	s_waitcnt vmcnt(15)
	v_mul_f32_e32 v18, 0x42800000, v64
	v_cvt_pk_fp8_f32 v16, v19, v20 op_sel:[0,0,1]
	s_waitcnt vmcnt(14)
	v_mul_f32_e32 v19, 0x42800000, v68
	v_mov_b32_e32 v17, v129
	v_cvt_pk_fp8_f32 v17, v18, v19
	s_waitcnt vmcnt(13)
	v_mul_f32_e32 v20, 0x42800000, v72
	s_waitcnt vmcnt(12)
	v_mul_f32_e32 v21, 0x42800000, v76
	s_waitcnt vmcnt(11)
	v_mul_f32_e32 v19, 0x42800000, v32
	v_cvt_pk_fp8_f32 v17, v20, v21 op_sel:[0,0,1]
	s_waitcnt vmcnt(10)
	v_mul_f32_e32 v20, 0x42800000, v36
	v_mov_b32_e32 v18, v129
	v_cvt_pk_fp8_f32 v18, v19, v20
	s_waitcnt vmcnt(7)
	v_mul_f32_e32 v0, 0x42800000, v0
	s_waitcnt vmcnt(6)
	v_mul_f32_e32 v4, 0x42800000, v4
	v_mov_b32_e32 v19, v129
	v_cvt_pk_fp8_f32 v19, v0, v4
	v_mul_f32_e32 v21, 0x42800000, v40
	v_mul_f32_e32 v22, 0x42800000, v44
	s_waitcnt vmcnt(5)
	v_mul_f32_e32 v8, 0x42800000, v8
	s_waitcnt vmcnt(4)
	v_mul_f32_e32 v12, 0x42800000, v12
	v_cvt_pk_fp8_f32 v18, v21, v22 op_sel:[0,0,1]
	v_cvt_pk_fp8_f32 v19, v8, v12 op_sel:[0,0,1]
	v_mul_f32_e32 v0, 0x42800000, v97
	v_mul_f32_e32 v4, 0x42800000, v101
	v_mul_f32_e32 v8, 0x42800000, v105
	ds_write_b128 v204, v[16:19] offset:32768
	v_mov_b32_e32 v16, v129
	v_cvt_pk_fp8_f32 v16, v0, v4
	v_mul_f32_e32 v0, 0x42800000, v65
	v_mul_f32_e32 v4, 0x42800000, v69
	v_mov_b32_e32 v17, v129
	v_cvt_pk_fp8_f32 v17, v0, v4
	v_mul_f32_e32 v0, 0x42800000, v33
	v_mul_f32_e32 v4, 0x42800000, v37
	v_mov_b32_e32 v18, v129
	v_cvt_pk_fp8_f32 v18, v0, v4
	v_mul_f32_e32 v0, 0x42800000, v1
	v_mul_f32_e32 v1, 0x42800000, v5
	v_mov_b32_e32 v19, v129
	v_cvt_pk_fp8_f32 v19, v0, v1
	v_mul_f32_e32 v12, 0x42800000, v125
	v_cvt_pk_fp8_f32 v16, v8, v12 op_sel:[0,0,1]
	v_mul_f32_e32 v8, 0x42800000, v73
	v_mul_f32_e32 v12, 0x42800000, v77
	v_cvt_pk_fp8_f32 v17, v8, v12 op_sel:[0,0,1]
	v_mul_f32_e32 v8, 0x42800000, v41
	v_mul_f32_e32 v12, 0x42800000, v45
	v_mul_f32_e32 v4, 0x42800000, v9
	v_mul_f32_e32 v5, 0x42800000, v13
	v_cvt_pk_fp8_f32 v18, v8, v12 op_sel:[0,0,1]
	v_cvt_pk_fp8_f32 v19, v4, v5 op_sel:[0,0,1]
	v_mul_f32_e32 v0, 0x42800000, v98
	v_mul_f32_e32 v1, 0x42800000, v102
	v_mul_f32_e32 v4, 0x42800000, v106
	ds_write_b128 v204, v[16:19] offset:32896
	v_mov_b32_e32 v16, v129
	v_cvt_pk_fp8_f32 v16, v0, v1
	v_mul_f32_e32 v0, 0x42800000, v66
	v_mul_f32_e32 v1, 0x42800000, v70
	v_mov_b32_e32 v17, v129
	v_cvt_pk_fp8_f32 v17, v0, v1
	v_mul_f32_e32 v0, 0x42800000, v34
	v_mul_f32_e32 v1, 0x42800000, v38
	v_mov_b32_e32 v18, v129
	v_cvt_pk_fp8_f32 v18, v0, v1
	v_mul_f32_e32 v0, 0x42800000, v2
	v_mul_f32_e32 v1, 0x42800000, v6
	v_mov_b32_e32 v19, v129
	v_mul_f32_e32 v5, 0x42800000, v126
	v_cvt_pk_fp8_f32 v19, v0, v1
	v_cvt_pk_fp8_f32 v16, v4, v5 op_sel:[0,0,1]
	v_mul_f32_e32 v4, 0x42800000, v74
	v_mul_f32_e32 v5, 0x42800000, v78
	v_cvt_pk_fp8_f32 v17, v4, v5 op_sel:[0,0,1]
	v_mul_f32_e32 v4, 0x42800000, v42
	v_mul_f32_e32 v5, 0x42800000, v46
	v_cvt_pk_fp8_f32 v18, v4, v5 op_sel:[0,0,1]
	v_mul_f32_e32 v2, 0x42800000, v10
	v_mul_f32_e32 v4, 0x42800000, v14
	v_cvt_pk_fp8_f32 v19, v2, v4 op_sel:[0,0,1]
	v_mul_f32_e32 v1, 0x42800000, v99
	v_mul_f32_e32 v2, 0x42800000, v103
	v_mov_b32_e32 v0, v129
	v_cvt_pk_fp8_f32 v0, v1, v2
	v_mul_f32_e32 v4, 0x42800000, v107
	v_mul_f32_e32 v5, 0x42800000, v127
	v_mul_f32_e32 v2, 0x42800000, v67
	v_cvt_pk_fp8_f32 v0, v4, v5 op_sel:[0,0,1]
	v_mul_f32_e32 v4, 0x42800000, v71
	v_mov_b32_e32 v1, v129
	v_cvt_pk_fp8_f32 v1, v2, v4
	v_mul_f32_e32 v5, 0x42800000, v75
	v_mul_f32_e32 v6, 0x42800000, v79
	v_mul_f32_e32 v4, 0x42800000, v35
	v_cvt_pk_fp8_f32 v1, v5, v6 op_sel:[0,0,1]
	v_mul_f32_e32 v5, 0x42800000, v39
	v_mov_b32_e32 v2, v129
	v_cvt_pk_fp8_f32 v2, v4, v5
	v_mul_f32_e32 v4, 0x42800000, v3
	v_mul_f32_e32 v5, 0x42800000, v7
	v_mov_b32_e32 v3, v129
	v_cvt_pk_fp8_f32 v3, v4, v5
	v_mul_f32_e32 v6, 0x42800000, v43
	v_mul_f32_e32 v8, 0x42800000, v47
	v_cvt_pk_fp8_f32 v2, v6, v8 op_sel:[0,0,1]
	v_mul_f32_e32 v6, 0x42800000, v11
	v_mul_f32_e32 v7, 0x42800000, v15
	v_cvt_pk_fp8_f32 v3, v6, v7 op_sel:[0,0,1]
	ds_write_b128 v204, v[16:19] offset:33024
	ds_write_b128 v204, v[0:3] offset:33152
	s_waitcnt lgkmcnt(0)
	s_barrier
	ds_read_b128 v[0:3], v205 offset:32768
	v_lshl_add_u64 v[4:5], v[140:141], 0, s[46:47]
	v_lshl_add_u64 v[6:7], v[4:5], 0, v[132:133]
	s_waitcnt lgkmcnt(0)
	global_store_dwordx4 v[6:7], v[0:3], off nt
	ds_read_b128 v[0:3], v206 offset:32768
	v_lshl_add_u64 v[6:7], v[4:5], 0, v[134:135]
	s_waitcnt lgkmcnt(0)
	global_store_dwordx4 v[6:7], v[0:3], off nt
	ds_read_b128 v[0:3], v207 offset:32768
	v_lshl_add_u64 v[6:7], v[4:5], 0, v[136:137]
	v_lshl_add_u64 v[4:5], v[4:5], 0, v[138:139]
	s_waitcnt lgkmcnt(0)
	global_store_dwordx4 v[6:7], v[0:3], off nt
	ds_read_b128 v[0:3], v208 offset:32768
	s_waitcnt lgkmcnt(0)
	global_store_dwordx4 v[4:5], v[0:3], off nt
	s_mov_b64 s[48:49], 0

; __device__ __forceinline__ void conv_queue(const Params& p, LAS unsigned char* lds, const int wave, const int cw, const int first, const int last, const int slot_off = LDS_MISC) {
;     ...
;         if (tid == 0) *slot = first + (int)atomicAdd(&p.ctl[cw], 1u);
;         __syncthreads();
;         const int it = *slot;
.LBB0_1251:
	s_or_b64 exec, exec, s[52:53]
	s_waitcnt vmcnt(0)
	v_readfirstlane_b32 s2, v1
	v_mov_b32_e32 v1, s13
	s_nop 0
	v_add_u32_e32 v0, s2, v0
	v_add_u32_e32 v0, 0x400, v0
	ds_write_b32 v1, v0

; __device__ __forceinline__ void conv_queue(const Params& p, LAS unsigned char* lds, const int wave, const int cw, const int first, const int last, const int slot_off = LDS_MISC) {
;     ...
;         if (tid == 0) *slot = first + (int)atomicAdd(&p.ctl[cw], 1u);
;         __syncthreads();
;         const int it = *slot;
.LBB0_1276:
	s_or_b64 exec, exec, s[50:51]
	s_waitcnt vmcnt(0)
	v_readfirstlane_b32 s2, v1
	v_mov_b32_e32 v1, s13
	s_nop 0
	v_add_u32_e32 v0, s2, v0
	v_add_u32_e32 v0, 0x400, v0
	ds_write_b32 v1, v0
